# weight-conversion tile loop unrolled x3 with renamed register sets (no rotation moves), counted vmcnt waits so the next two tiles' loads stay in flight; all 6 instances
# speedup vs baseline: 1.0089x; 1.0085x over previous
; #define LAS __attribute__((address_space(3)))
; __device__ __forceinline__ unsigned cvt_pk_bf16(float lo, float hi) { const bf16x2_t r = __builtin_convertvector((f32x2_t){lo, hi}, bf16x2_t); return __builtin_bit_cast(unsigned, r); }
; __device__ __forceinline__ void cvt_range(const MkArgs& a, LAS unsigned char* lds, const int tid, const int first, const int step, const int end, const bool deferred) {
;     ...
;         for (int i = 0; i < 8; ++i) {
;             u32x2 p; p[0] = cvt_pk_bf16(v[i][0], v[i][1]); p[1] = cvt_pk_bf16(v[i][2], v[i][3]);
;             *(LAS u32x2*)(lds + (kk + 16 * i) * RS + c4 * 8) = p;
;         }
;         __syncthreads();
;         {
;             typedef short s16x4_t __attribute__((ext_vector_type(4)));
;             const int ln = tid & 63, wq = tid >> 6, li = ln & 15, gq = li >> 2, gp = li & 3, G4 = ln >> 4;
; #pragma unroll
;             for (int i = 0; i < 4; ++i) {
;                 const int nb = wq, k8 = 2 * (G4 + 4 * (i >> 1)) + (i & 1);
;                 const LAS unsigned char* p0 = lds + (8 * k8 + gq) * RS + (16 * nb + 4 * gp) * 2;
;                 const s16x4_t x0 = __builtin_amdgcn_ds_read_tr16_b64_v4i16((LAS s16x4_t*)p0), x1 = __builtin_amdgcn_ds_read_tr16_b64_v4i16((LAS s16x4_t*)(p0 + 4 * RS));
;                 typedef short s16x8_t __attribute__((ext_vector_type(8)));
;                 const s16x8_t o8 = (s16x8_t){x0[0], x0[1], x0[2], x0[3], x1[0], x1[1], x1[2], x1[3]};
;                 *(u32x4*)(dst + (size_t)(16 * nb + li) * K + k8 * 8) = __builtin_bit_cast(u32x4, o8);
;             }
;         }
;         __syncthreads();
;         t += step; src = srcn; dst = dstn; ld = ldn; K = Kn; srcn = srcm; dstn = dstm; ldn = ldm; Kn = Km;
; #pragma unroll
;         for (int i = 0; i < 8; ++i) { v[i] = vn[i]; vn[i] = vm[i]; }
.LBB0_177:
	s_waitcnt vmcnt(23)
	v_cvt_pk_bf16_f32 v4, v4, v5
	v_cvt_pk_bf16_f32 v5, v6, v7
	s_waitcnt vmcnt(22)
	v_cvt_pk_bf16_f32 v0, v0, v1
	v_cvt_pk_bf16_f32 v1, v2, v3
	ds_write2st64_b64 v118, v[4:5], v[0:1] offset1:10
	s_waitcnt vmcnt(21)
	v_cvt_pk_bf16_f32 v0, v12, v13
	v_cvt_pk_bf16_f32 v1, v14, v15
	s_waitcnt vmcnt(20)
	v_cvt_pk_bf16_f32 v2, v8, v9
	v_cvt_pk_bf16_f32 v3, v10, v11
	ds_write2st64_b64 v118, v[0:1], v[2:3] offset0:20 offset1:30
	s_waitcnt vmcnt(19)
	v_cvt_pk_bf16_f32 v0, v20, v21
	v_cvt_pk_bf16_f32 v1, v22, v23
	s_waitcnt vmcnt(18)
	v_cvt_pk_bf16_f32 v2, v16, v17
	v_cvt_pk_bf16_f32 v3, v18, v19
	ds_write2st64_b64 v118, v[0:1], v[2:3] offset0:40 offset1:50
	s_waitcnt vmcnt(17)
	v_cvt_pk_bf16_f32 v0, v28, v29
	v_cvt_pk_bf16_f32 v1, v30, v31
	s_waitcnt vmcnt(16)
	v_cvt_pk_bf16_f32 v2, v24, v25
	v_cvt_pk_bf16_f32 v3, v26, v27
	ds_write2st64_b64 v118, v[0:1], v[2:3] offset0:60 offset1:70
	v_mul_lo_u32 v2, s3, v100
	v_mul_lo_u32 v3, s2, v99
	v_mad_u64_u32 v[0:1], s[2:3], s2, v100, 0
	v_add3_u32 v1, v1, v3, v2
	s_waitcnt lgkmcnt(0)
	s_barrier
	v_lshl_add_u64 v[16:17], v[0:1], 1, s[0:1]
	ds_read_b64_tr_b16 v[0:1], v119
	ds_read_b64_tr_b16 v[2:3], v119 offset:1280
	ds_read_b64_tr_b16 v[4:5], v120
	ds_read_b64_tr_b16 v[6:7], v120 offset:1280
	ds_read_b64_tr_b16 v[8:9], v121
	ds_read_b64_tr_b16 v[10:11], v121 offset:1280
	ds_read_b64_tr_b16 v[12:13], v122
	ds_read_b64_tr_b16 v[14:15], v122 offset:1280
	v_mov_b32_e32 v117, v97
	v_lshl_add_u64 v[16:17], v[16:17], 0, v[116:117]
	s_waitcnt lgkmcnt(6)
	global_store_dwordx4 v[16:17], v[0:3], off
	s_waitcnt lgkmcnt(4)
	global_store_dwordx4 v[16:17], v[4:7], off offset:16
	s_waitcnt lgkmcnt(2)
	global_store_dwordx4 v[16:17], v[8:11], off offset:128
	s_waitcnt lgkmcnt(0)
	global_store_dwordx4 v[16:17], v[12:15], off offset:144
	s_add_i32 s34, s34, s93
	s_cmpk_gt_i32 s34, 0x2bff
	s_mov_b64 s[2:3], s[14:15]
	s_mov_b64 s[0:1], s[10:11]
	s_barrier
	s_cbranch_scc1 .LBB0_195

; #define LAS __attribute__((address_space(3)))
; __device__ __forceinline__ unsigned cvt_pk_bf16(float lo, float hi) { const bf16x2_t r = __builtin_convertvector((f32x2_t){lo, hi}, bf16x2_t); return __builtin_bit_cast(unsigned, r); }
; __device__ __forceinline__ void cvt_range(const MkArgs& a, LAS unsigned char* lds, const int tid, const int first, const int step, const int end, const bool deferred) {
;     ...
;         if (tm < end) { cvt_decode(cvt_map(tm, deferred), w_in, w_out, w_eg, w_eu, w_ed, WinT, WoutT, WguT, WdT, srcm, dstm, ldm, Km);
; #pragma unroll
;             for (int i = 0; i < 8; ++i) vm[i] = __builtin_nontemporal_load((const f32x4*)(srcm + (size_t)(kk + 16 * i) * ldm + c4 * 4)); }
; #pragma unroll
;         for (int i = 0; i < 8; ++i) {
;             u32x2 p; p[0] = cvt_pk_bf16(v[i][0], v[i][1]); p[1] = cvt_pk_bf16(v[i][2], v[i][3]);
;             *(LAS u32x2*)(lds + (kk + 16 * i) * RS + c4 * 8) = p;
;         }
;         __syncthreads();
;         {
;             typedef short s16x4_t __attribute__((ext_vector_type(4)));
;             const int ln = tid & 63, wq = tid >> 6, li = ln & 15, gq = li >> 2, gp = li & 3, G4 = ln >> 4;
; #pragma unroll
;             for (int i = 0; i < 4; ++i) {
;                 const int nb = wq, k8 = 2 * (G4 + 4 * (i >> 1)) + (i & 1);
;                 const LAS unsigned char* p0 = lds + (8 * k8 + gq) * RS + (16 * nb + 4 * gp) * 2;
;                 const s16x4_t x0 = __builtin_amdgcn_ds_read_tr16_b64_v4i16((LAS s16x4_t*)p0), x1 = __builtin_amdgcn_ds_read_tr16_b64_v4i16((LAS s16x4_t*)(p0 + 4 * RS));
;                 typedef short s16x8_t __attribute__((ext_vector_type(8)));
;                 const s16x8_t o8 = (s16x8_t){x0[0], x0[1], x0[2], x0[3], x1[0], x1[1], x1[2], x1[3]};
;                 *(u32x4*)(dst + (size_t)(16 * nb + li) * K + k8 * 8) = __builtin_bit_cast(u32x4, o8);
;             }
;         }
;         __syncthreads();
;         t += step; src = srcn; dst = dstn; ld = ldn; K = Kn; srcn = srcm; dstn = dstm; ldn = ldm; Kn = Km;
.Lmy_cv0_strict_1:
	s_waitcnt vmcnt(0)
	s_branch .Lmy_cv0_1_177
.Lmy_cv0_1_176:
	v_lshl_add_u64 v[28:29], s[16:17], 0, v[96:97]
	v_mul_lo_u32 v6, s19, v98
	v_mul_lo_u32 v7, s18, v101
	v_mad_u64_u32 v[4:5], s[16:17], s18, v98, 0
	v_mul_lo_u32 v10, s19, v104
	v_mul_lo_u32 v11, s18, v105
	v_mad_u64_u32 v[8:9], s[16:17], s18, v104, 0
	v_mul_lo_u32 v22, s19, v108
	v_mul_lo_u32 v23, s18, v109
	v_mad_u64_u32 v[20:21], s[16:17], s18, v108, 0
	v_mul_lo_u32 v24, s19, v112
	v_mul_lo_u32 v25, s18, v113
	v_mad_u64_u32 v[30:31], s[16:17], s18, v112, 0
	v_add3_u32 v5, v5, v7, v6
	v_mul_lo_u32 v0, s19, v102
	v_mul_lo_u32 v1, s18, v103
	v_mad_u64_u32 v[6:7], s[16:17], s18, v102, 0
	v_add3_u32 v9, v9, v11, v10
	v_mul_lo_u32 v12, s19, v106
	v_mul_lo_u32 v13, s18, v107
	v_mad_u64_u32 v[10:11], s[16:17], s18, v106, 0
	v_add3_u32 v21, v21, v23, v22
	v_mul_lo_u32 v16, s19, v110
	v_mul_lo_u32 v17, s18, v111
	v_mad_u64_u32 v[22:23], s[16:17], s18, v110, 0
	v_add3_u32 v31, v31, v25, v24
	v_mul_lo_u32 v26, s19, v114
	v_mul_lo_u32 v27, s18, v115
	v_mad_u64_u32 v[24:25], s[16:17], s18, v114, 0
	v_add3_u32 v7, v7, v1, v0
	v_add3_u32 v11, v11, v13, v12
	v_add3_u32 v23, v23, v17, v16
	v_add3_u32 v25, v25, v27, v26
	v_lshl_add_u64 v[4:5], v[4:5], 2, v[28:29]
	v_lshl_add_u64 v[0:1], v[6:7], 2, v[28:29]
	v_lshl_add_u64 v[8:9], v[8:9], 2, v[28:29]
	v_lshl_add_u64 v[10:11], v[10:11], 2, v[28:29]
	v_lshl_add_u64 v[20:21], v[20:21], 2, v[28:29]
	v_lshl_add_u64 v[16:17], v[22:23], 2, v[28:29]
	v_lshl_add_u64 v[30:31], v[30:31], 2, v[28:29]
	v_lshl_add_u64 v[24:25], v[24:25], 2, v[28:29]
	global_load_dwordx4 v[4:7], v[4:5], off nt
	s_nop 0
	global_load_dwordx4 v[0:3], v[0:1], off nt
	s_nop 0
	global_load_dwordx4 v[12:15], v[8:9], off nt
	s_nop 0
	global_load_dwordx4 v[8:11], v[10:11], off nt
	s_nop 0
	global_load_dwordx4 v[20:23], v[20:21], off nt
	s_nop 0
	global_load_dwordx4 v[16:19], v[16:17], off nt
	s_nop 0
	global_load_dwordx4 v[28:31], v[30:31], off nt
	s_nop 0
	global_load_dwordx4 v[24:27], v[24:25], off nt
.Lmy_cv0_1_177:
	s_waitcnt vmcnt(23)
	v_cvt_pk_bf16_f32 v36, v36, v37
	v_cvt_pk_bf16_f32 v37, v38, v39
	s_waitcnt vmcnt(22)
	v_cvt_pk_bf16_f32 v32, v32, v33
	v_cvt_pk_bf16_f32 v33, v34, v35
	ds_write2st64_b64 v118, v[36:37], v[32:33] offset1:10
	s_waitcnt vmcnt(21)
	v_cvt_pk_bf16_f32 v32, v44, v45
	v_cvt_pk_bf16_f32 v33, v46, v47
	s_waitcnt vmcnt(20)
	v_cvt_pk_bf16_f32 v34, v40, v41
	v_cvt_pk_bf16_f32 v35, v42, v43
	ds_write2st64_b64 v118, v[32:33], v[34:35] offset0:20 offset1:30
	s_waitcnt vmcnt(19)
	v_cvt_pk_bf16_f32 v32, v52, v53
	v_cvt_pk_bf16_f32 v33, v54, v55
	s_waitcnt vmcnt(18)
	v_cvt_pk_bf16_f32 v34, v48, v49
	v_cvt_pk_bf16_f32 v35, v50, v51
	ds_write2st64_b64 v118, v[32:33], v[34:35] offset0:40 offset1:50
	s_waitcnt vmcnt(17)
	v_cvt_pk_bf16_f32 v32, v60, v61
	v_cvt_pk_bf16_f32 v33, v62, v63
	s_waitcnt vmcnt(16)
	v_cvt_pk_bf16_f32 v34, v56, v57
	v_cvt_pk_bf16_f32 v35, v58, v59
	ds_write2st64_b64 v118, v[32:33], v[34:35] offset0:60 offset1:70
	v_mul_lo_u32 v34, s3, v100
	v_mul_lo_u32 v35, s2, v99
	v_mad_u64_u32 v[32:33], s[2:3], s2, v100, 0
	v_add3_u32 v33, v33, v35, v34
	s_waitcnt lgkmcnt(0)
	s_barrier
	v_lshl_add_u64 v[48:49], v[32:33], 1, s[0:1]
	ds_read_b64_tr_b16 v[32:33], v119
	ds_read_b64_tr_b16 v[34:35], v119 offset:1280
	ds_read_b64_tr_b16 v[36:37], v120
	ds_read_b64_tr_b16 v[38:39], v120 offset:1280
	ds_read_b64_tr_b16 v[40:41], v121
	ds_read_b64_tr_b16 v[42:43], v121 offset:1280
	ds_read_b64_tr_b16 v[44:45], v122
	ds_read_b64_tr_b16 v[46:47], v122 offset:1280
	v_mov_b32_e32 v117, v97
	v_lshl_add_u64 v[48:49], v[48:49], 0, v[116:117]
	s_waitcnt lgkmcnt(6)
	global_store_dwordx4 v[48:49], v[32:35], off
	s_waitcnt lgkmcnt(4)
	global_store_dwordx4 v[48:49], v[36:39], off offset:16
	s_waitcnt lgkmcnt(2)
	global_store_dwordx4 v[48:49], v[40:43], off offset:128
	s_waitcnt lgkmcnt(0)
	global_store_dwordx4 v[48:49], v[44:47], off offset:144
	s_add_i32 s34, s34, s93
	s_cmpk_gt_i32 s34, 0x2bff
	s_mov_b64 s[2:3], s[14:15]
	s_mov_b64 s[0:1], s[10:11]
	s_barrier
	s_cbranch_scc1 .LBB0_195

; #define LAS __attribute__((address_space(3)))
; __device__ __forceinline__ unsigned cvt_pk_bf16(float lo, float hi) { const bf16x2_t r = __builtin_convertvector((f32x2_t){lo, hi}, bf16x2_t); return __builtin_bit_cast(unsigned, r); }
; __device__ __forceinline__ void cvt_range(const MkArgs& a, LAS unsigned char* lds, const int tid, const int first, const int step, const int end, const bool deferred) {
;     ...
;         if (tm < end) { cvt_decode(cvt_map(tm, deferred), w_in, w_out, w_eg, w_eu, w_ed, WinT, WoutT, WguT, WdT, srcm, dstm, ldm, Km);
; #pragma unroll
;             for (int i = 0; i < 8; ++i) vm[i] = __builtin_nontemporal_load((const f32x4*)(srcm + (size_t)(kk + 16 * i) * ldm + c4 * 4)); }
; #pragma unroll
;         for (int i = 0; i < 8; ++i) {
;             u32x2 p; p[0] = cvt_pk_bf16(v[i][0], v[i][1]); p[1] = cvt_pk_bf16(v[i][2], v[i][3]);
;             *(LAS u32x2*)(lds + (kk + 16 * i) * RS + c4 * 8) = p;
;         }
;         __syncthreads();
;         {
;             typedef short s16x4_t __attribute__((ext_vector_type(4)));
;             const int ln = tid & 63, wq = tid >> 6, li = ln & 15, gq = li >> 2, gp = li & 3, G4 = ln >> 4;
; #pragma unroll
;             for (int i = 0; i < 4; ++i) {
;                 const int nb = wq, k8 = 2 * (G4 + 4 * (i >> 1)) + (i & 1);
;                 const LAS unsigned char* p0 = lds + (8 * k8 + gq) * RS + (16 * nb + 4 * gp) * 2;
;                 const s16x4_t x0 = __builtin_amdgcn_ds_read_tr16_b64_v4i16((LAS s16x4_t*)p0), x1 = __builtin_amdgcn_ds_read_tr16_b64_v4i16((LAS s16x4_t*)(p0 + 4 * RS));
;                 typedef short s16x8_t __attribute__((ext_vector_type(8)));
;                 const s16x8_t o8 = (s16x8_t){x0[0], x0[1], x0[2], x0[3], x1[0], x1[1], x1[2], x1[3]};
;                 *(u32x4*)(dst + (size_t)(16 * nb + li) * K + k8 * 8) = __builtin_bit_cast(u32x4, o8);
;             }
;         }
;         __syncthreads();
;         t += step; src = srcn; dst = dstn; ld = ldn; K = Kn; srcn = srcm; dstn = dstm; ldn = ldm; Kn = Km;
.Lmy_cv0_2_176:
	v_lshl_add_u64 v[60:61], s[16:17], 0, v[96:97]
	v_mul_lo_u32 v38, s19, v98
	v_mul_lo_u32 v39, s18, v101
	v_mad_u64_u32 v[36:37], s[16:17], s18, v98, 0
	v_mul_lo_u32 v42, s19, v104
	v_mul_lo_u32 v43, s18, v105
	v_mad_u64_u32 v[40:41], s[16:17], s18, v104, 0
	v_mul_lo_u32 v54, s19, v108
	v_mul_lo_u32 v55, s18, v109
	v_mad_u64_u32 v[52:53], s[16:17], s18, v108, 0
	v_mul_lo_u32 v56, s19, v112
	v_mul_lo_u32 v57, s18, v113
	v_mad_u64_u32 v[62:63], s[16:17], s18, v112, 0
	v_add3_u32 v37, v37, v39, v38
	v_mul_lo_u32 v32, s19, v102
	v_mul_lo_u32 v33, s18, v103
	v_mad_u64_u32 v[38:39], s[16:17], s18, v102, 0
	v_add3_u32 v41, v41, v43, v42
	v_mul_lo_u32 v44, s19, v106
	v_mul_lo_u32 v45, s18, v107
	v_mad_u64_u32 v[42:43], s[16:17], s18, v106, 0
	v_add3_u32 v53, v53, v55, v54
	v_mul_lo_u32 v48, s19, v110
	v_mul_lo_u32 v49, s18, v111
	v_mad_u64_u32 v[54:55], s[16:17], s18, v110, 0
	v_add3_u32 v63, v63, v57, v56
	v_mul_lo_u32 v58, s19, v114
	v_mul_lo_u32 v59, s18, v115
	v_mad_u64_u32 v[56:57], s[16:17], s18, v114, 0
	v_add3_u32 v39, v39, v33, v32
	v_add3_u32 v43, v43, v45, v44
	v_add3_u32 v55, v55, v49, v48
	v_add3_u32 v57, v57, v59, v58
	v_lshl_add_u64 v[36:37], v[36:37], 2, v[60:61]
	v_lshl_add_u64 v[32:33], v[38:39], 2, v[60:61]
	v_lshl_add_u64 v[40:41], v[40:41], 2, v[60:61]
	v_lshl_add_u64 v[42:43], v[42:43], 2, v[60:61]
	v_lshl_add_u64 v[52:53], v[52:53], 2, v[60:61]
	v_lshl_add_u64 v[48:49], v[54:55], 2, v[60:61]
	v_lshl_add_u64 v[62:63], v[62:63], 2, v[60:61]
	v_lshl_add_u64 v[56:57], v[56:57], 2, v[60:61]
	global_load_dwordx4 v[36:39], v[36:37], off nt
	s_nop 0
	global_load_dwordx4 v[32:35], v[32:33], off nt
	s_nop 0
	global_load_dwordx4 v[44:47], v[40:41], off nt
	s_nop 0
	global_load_dwordx4 v[40:43], v[42:43], off nt
	s_nop 0
	global_load_dwordx4 v[52:55], v[52:53], off nt
	s_nop 0
	global_load_dwordx4 v[48:51], v[48:49], off nt
	s_nop 0
	global_load_dwordx4 v[60:63], v[62:63], off nt
	s_nop 0
	global_load_dwordx4 v[56:59], v[56:57], off nt
.Lmy_cv0_2_177:
	s_waitcnt vmcnt(23)
	v_cvt_pk_bf16_f32 v64, v64, v65
	v_cvt_pk_bf16_f32 v65, v66, v67
	s_waitcnt vmcnt(22)
	v_cvt_pk_bf16_f32 v68, v68, v69
	v_cvt_pk_bf16_f32 v69, v70, v71
	ds_write2st64_b64 v118, v[64:65], v[68:69] offset1:10
	s_waitcnt vmcnt(21)
	v_cvt_pk_bf16_f32 v68, v76, v77
	v_cvt_pk_bf16_f32 v69, v78, v79
	s_waitcnt vmcnt(20)
	v_cvt_pk_bf16_f32 v70, v72, v73
	v_cvt_pk_bf16_f32 v71, v74, v75
	ds_write2st64_b64 v118, v[68:69], v[70:71] offset0:20 offset1:30
	s_waitcnt vmcnt(19)
	v_cvt_pk_bf16_f32 v68, v80, v81
	v_cvt_pk_bf16_f32 v69, v82, v83
	s_waitcnt vmcnt(18)
	v_cvt_pk_bf16_f32 v70, v84, v85
	v_cvt_pk_bf16_f32 v71, v86, v87
	ds_write2st64_b64 v118, v[68:69], v[70:71] offset0:40 offset1:50
	s_waitcnt vmcnt(17)
	v_cvt_pk_bf16_f32 v68, v88, v89
	v_cvt_pk_bf16_f32 v69, v90, v91
	s_waitcnt vmcnt(16)
	v_cvt_pk_bf16_f32 v70, v92, v93
	v_cvt_pk_bf16_f32 v71, v94, v95
	ds_write2st64_b64 v118, v[68:69], v[70:71] offset0:60 offset1:70
	v_mul_lo_u32 v70, s3, v100
	v_mul_lo_u32 v71, s2, v99
	v_mad_u64_u32 v[68:69], s[2:3], s2, v100, 0
	v_add3_u32 v69, v69, v71, v70
	s_waitcnt lgkmcnt(0)
	s_barrier
	v_lshl_add_u64 v[84:85], v[68:69], 1, s[0:1]
	ds_read_b64_tr_b16 v[68:69], v119
	ds_read_b64_tr_b16 v[70:71], v119 offset:1280
	ds_read_b64_tr_b16 v[64:65], v120
	ds_read_b64_tr_b16 v[66:67], v120 offset:1280
	ds_read_b64_tr_b16 v[72:73], v121
	ds_read_b64_tr_b16 v[74:75], v121 offset:1280
	ds_read_b64_tr_b16 v[76:77], v122
	ds_read_b64_tr_b16 v[78:79], v122 offset:1280
	v_mov_b32_e32 v117, v97
	v_lshl_add_u64 v[84:85], v[84:85], 0, v[116:117]
	s_waitcnt lgkmcnt(6)
	global_store_dwordx4 v[84:85], v[68:71], off
	s_waitcnt lgkmcnt(4)
	global_store_dwordx4 v[84:85], v[64:67], off offset:16
	s_waitcnt lgkmcnt(2)
	global_store_dwordx4 v[84:85], v[72:75], off offset:128
	s_waitcnt lgkmcnt(0)
	global_store_dwordx4 v[84:85], v[76:79], off offset:144
	s_add_i32 s34, s34, s93
	s_cmpk_gt_i32 s34, 0x2bff
	s_mov_b64 s[2:3], s[14:15]
	s_mov_b64 s[0:1], s[10:11]
	s_barrier
	s_cbranch_scc1 .LBB0_195

; #define LAS __attribute__((address_space(3)))
; __device__ __forceinline__ void cvt_decode(int t, const float* w_in, const float* w_out, const float* w_eg, const float* w_eu, const float* w_ed,
;                                            bf16_t* WinT, bf16_t* WoutT, bf16_t* WguT, bf16_t* WdT, const float*& s_, bf16_t*& d_, int& ld_, int& K_) {
;     if (t < 2 * NT_G) { const int which = t / NT_G, t3 = t % NT_G, le = t3 / 128, r = t3 % 128, kt = r / 8, nt = r % 8;
;         s_ = (which ? w_eu : w_eg) + (size_t)le * DM * DEXP + (size_t)kt * 128 * DEXP + nt * 128; ld_ = DEXP; K_ = DM;
;         d_ = WguT + (size_t)le * 2048 * DM + (size_t)(nt * 256 + which * 128) * DM + kt * 128; }
;     else if (t < 2 * NT_G + NT_D) { const int t2 = t - 2 * NT_G, le = t2 / 128, r = t2 % 128, kt = r / 16, nt = r % 16;
; __device__ __forceinline__ void cvt_range(const MkArgs& a, LAS unsigned char* lds, const int tid, const int first, const int step, const int end, const bool deferred) {
;     ...
;         for (int i = 0; i < 8; ++i) {
;             u32x2 p; p[0] = cvt_pk_bf16(v[i][0], v[i][1]); p[1] = cvt_pk_bf16(v[i][2], v[i][3]);
;             *(LAS u32x2*)(lds + (kk + 16 * i) * RS + c4 * 8) = p;
;         }
;         __syncthreads();
;         {
;             typedef short s16x4_t __attribute__((ext_vector_type(4)));
;             const int ln = tid & 63, wq = tid >> 6, li = ln & 15, gq = li >> 2, gp = li & 3, G4 = ln >> 4;
; #pragma unroll
;             for (int i = 0; i < 4; ++i) {
;                 const int nb = wq, k8 = 2 * (G4 + 4 * (i >> 1)) + (i & 1);
;                 const LAS unsigned char* p0 = lds + (8 * k8 + gq) * RS + (16 * nb + 4 * gp) * 2;
;                 const s16x4_t x0 = __builtin_amdgcn_ds_read_tr16_b64_v4i16((LAS s16x4_t*)p0), x1 = __builtin_amdgcn_ds_read_tr16_b64_v4i16((LAS s16x4_t*)(p0 + 4 * RS));
;                 typedef short s16x8_t __attribute__((ext_vector_type(8)));
;                 const s16x8_t o8 = (s16x8_t){x0[0], x0[1], x0[2], x0[3], x1[0], x1[1], x1[2], x1[3]};
;                 *(u32x4*)(dst + (size_t)(16 * nb + li) * K + k8 * 8) = __builtin_bit_cast(u32x4, o8);
;             }
;         }
;         __syncthreads();
;         t += step; src = srcn; dst = dstn; ld = ldn; K = Kn; srcn = srcm; dstn = dstm; ldn = ldm; Kn = Km;
.LBB0_668:
	s_waitcnt vmcnt(23)
	v_cvt_pk_bf16_f32 v0, v0, v1
	v_cvt_pk_bf16_f32 v1, v2, v3
	s_waitcnt vmcnt(22)
	v_cvt_pk_bf16_f32 v2, v4, v5
	v_cvt_pk_bf16_f32 v3, v6, v7
	ds_write2st64_b64 v116, v[0:1], v[2:3] offset1:10
	s_waitcnt vmcnt(21)
	v_cvt_pk_bf16_f32 v0, v8, v9
	v_cvt_pk_bf16_f32 v1, v10, v11
	s_waitcnt vmcnt(20)
	v_cvt_pk_bf16_f32 v2, v12, v13
	v_cvt_pk_bf16_f32 v3, v14, v15
	ds_write2st64_b64 v116, v[0:1], v[2:3] offset0:20 offset1:30
	s_waitcnt vmcnt(19)
	v_cvt_pk_bf16_f32 v0, v16, v17
	v_cvt_pk_bf16_f32 v1, v18, v19
	s_waitcnt vmcnt(18)
	v_cvt_pk_bf16_f32 v2, v20, v21
	v_cvt_pk_bf16_f32 v3, v22, v23
	ds_write2st64_b64 v116, v[0:1], v[2:3] offset0:40 offset1:50
	s_waitcnt vmcnt(17)
	v_cvt_pk_bf16_f32 v0, v24, v25
	v_cvt_pk_bf16_f32 v1, v26, v27
	s_waitcnt vmcnt(16)
	v_cvt_pk_bf16_f32 v2, v28, v29
	v_cvt_pk_bf16_f32 v3, v30, v31
	ds_write2st64_b64 v116, v[0:1], v[2:3] offset0:60 offset1:70
	v_mul_lo_u32 v2, s9, v114
	v_mul_lo_u32 v3, s8, v115
	v_mad_u64_u32 v[0:1], s[8:9], s8, v114, 0
	v_add3_u32 v1, v1, v3, v2
	s_waitcnt lgkmcnt(0)
	s_barrier
	v_lshl_add_u64 v[16:17], v[0:1], 1, s[6:7]
	ds_read_b64_tr_b16 v[0:1], v117
	ds_read_b64_tr_b16 v[2:3], v117 offset:1280
	ds_read_b64_tr_b16 v[4:5], v118
	ds_read_b64_tr_b16 v[6:7], v118 offset:1280
	ds_read_b64_tr_b16 v[8:9], v119
	ds_read_b64_tr_b16 v[10:11], v119 offset:1280
	ds_read_b64_tr_b16 v[12:13], v120
	ds_read_b64_tr_b16 v[14:15], v120 offset:1280
	v_lshl_add_u64 v[16:17], v[16:17], 0, v[162:163]
	s_waitcnt lgkmcnt(6)
	global_store_dwordx4 v[16:17], v[0:3], off
	s_waitcnt lgkmcnt(4)
	global_store_dwordx4 v[16:17], v[4:7], off offset:16
	s_waitcnt lgkmcnt(2)
	global_store_dwordx4 v[16:17], v[8:11], off offset:128
	s_waitcnt lgkmcnt(0)
	global_store_dwordx4 v[16:17], v[12:15], off offset:144
	s_add_i32 s18, s18, 1
	s_cmp_lt_i32 s18, s26
	s_mov_b64 s[8:9], s[24:25]
	s_mov_b64 s[6:7], s[22:23]
	s_barrier
	s_cbranch_scc0 .LBB0_671
.Lmy_cv1_1_669:
	s_mov_b64 s[24:25], s[4:5]
	s_add_i32 s4, s18, 2
	s_mov_b64 s[22:23], s[2:3]
	s_mov_b64 s[2:3], 0
	s_cmp_ge_i32 s4, s26
	s_mov_b64 s[4:5], 0
	s_cbranch_scc1 .Lmy_cv1_strict_1
	s_cmpk_lt_i32 s18, 0xffe
	s_cselect_b32 s2, 0x1000, s63
	s_add_i32 s27, s2, s18
	s_add_i32 s2, s27, 2
	s_ashr_i32 s3, s2, 31
	s_lshr_b32 s3, s3, 19
	s_add_i32 s3, s2, s3
	s_ashr_i32 s29, s3, 13
	s_and_b32 s3, s3, 0xe000
	s_sub_i32 s28, s2, s3
	s_sext_i32_i16 s2, s28
	s_bfe_u32 s2, s2, 0x70018
	s_add_i32 s30, s28, s2
	s_sext_i32_i16 s2, s30
	s_lshr_b32 s2, s2, 7
	s_bfe_i64 s[2:3], s[2:3], 0x100000
	s_lshl_b64 s[4:5], s[2:3], 23
	s_add_u32 s31, s60, s4
	s_addc_u32 s33, s61, s5
	s_and_b32 s2, s30, 0xff80
	s_sub_i32 s2, s28, s2
	s_bfe_i32 s3, s2, 0x80000
	s_bfe_u32 s3, s3, 0x3000c
	s_add_i32 s3, s2, s3
	s_bfe_i32 s28, s3, 0x80000
	s_and_b32 s3, s3, 0xf8
	s_sub_i32 s2, s2, s3
	s_sext_i32_i8 s30, s2
	s_lshl_b32 s2, s30, 8
	s_lshl_b32 s3, s29, 7
	s_add_i32 s2, s2, s3
	s_sext_i32_i16 s28, s28
	s_ashr_i32 s3, s2, 31
	s_lshr_b32 s28, s28, 3
	s_lshl_b64 s[2:3], s[2:3], 12
	s_add_u32 s29, s31, s2
	s_addc_u32 s31, s33, s3
	s_lshl_b32 s2, s28, 7
	s_ashr_i32 s3, s2, 31
	s_lshl_b64 s[2:3], s[2:3], 1
	s_add_u32 s2, s29, s2
	s_addc_u32 s3, s31, s3
	s_addk_i32 s27, 0x2001
	s_cmpk_lt_u32 s27, 0x3fff
	s_cselect_b32 s29, s58, s84
	s_cselect_b32 s27, s59, s85
	s_add_u32 s29, s29, s4
	s_addc_u32 s27, s27, s5
	s_bfe_i64 s[4:5], s[28:29], 0x100000
	s_lshl_b64 s[4:5], s[4:5], 19
	s_add_u32 s28, s29, s4
	s_addc_u32 s27, s27, s5
	s_lshl_b32 s4, s30, 7
	s_ashr_i32 s5, s4, 31
	s_lshl_b64 s[4:5], s[4:5], 2
	s_add_u32 s4, s28, s4
	s_addc_u32 s5, s27, s5
	v_mov_b32_e32 v113, v163
	v_lshl_add_u64 v[28:29], s[4:5], 0, v[112:113]
	v_lshl_add_u64 v[4:5], v[28:29], 0, v[96:97]
	v_lshl_add_u64 v[6:7], v[28:29], 0, v[98:99]
	v_lshl_add_u64 v[12:13], v[28:29], 0, v[100:101]
	v_lshl_add_u64 v[14:15], v[28:29], 0, v[102:103]
	v_lshl_add_u64 v[20:21], v[28:29], 0, v[104:105]
	v_lshl_add_u64 v[22:23], v[28:29], 0, v[106:107]
	v_lshl_add_u64 v[30:31], v[28:29], 0, v[108:109]
	v_lshl_add_u64 v[28:29], v[28:29], 0, v[110:111]
	global_load_dwordx4 v[0:3], v[4:5], off nt
	s_nop 0
	global_load_dwordx4 v[4:7], v[6:7], off nt
	s_nop 0
	global_load_dwordx4 v[8:11], v[12:13], off nt
	s_nop 0
	global_load_dwordx4 v[12:15], v[14:15], off nt
	s_nop 0
	global_load_dwordx4 v[16:19], v[20:21], off nt
	s_nop 0
	global_load_dwordx4 v[20:23], v[22:23], off nt
	s_nop 0
	global_load_dwordx4 v[24:27], v[30:31], off nt
	s_nop 0
	global_load_dwordx4 v[28:31], v[28:29], off nt
	s_mov_b64 s[4:5], 0x800
	s_branch .Lmy_cv1_1_668

; #define LAS __attribute__((address_space(3)))
; __device__ __forceinline__ unsigned cvt_pk_bf16(float lo, float hi) { const bf16x2_t r = __builtin_convertvector((f32x2_t){lo, hi}, bf16x2_t); return __builtin_bit_cast(unsigned, r); }
; __device__ __forceinline__ void cvt_range(const MkArgs& a, LAS unsigned char* lds, const int tid, const int first, const int step, const int end, const bool deferred) {
;     ...
;         if (tm < end) { cvt_decode(cvt_map(tm, deferred), w_in, w_out, w_eg, w_eu, w_ed, WinT, WoutT, WguT, WdT, srcm, dstm, ldm, Km);
; #pragma unroll
;             for (int i = 0; i < 8; ++i) vm[i] = __builtin_nontemporal_load((const f32x4*)(srcm + (size_t)(kk + 16 * i) * ldm + c4 * 4)); }
; #pragma unroll
;         for (int i = 0; i < 8; ++i) {
;             u32x2 p; p[0] = cvt_pk_bf16(v[i][0], v[i][1]); p[1] = cvt_pk_bf16(v[i][2], v[i][3]);
;             *(LAS u32x2*)(lds + (kk + 16 * i) * RS + c4 * 8) = p;
;         }
;         __syncthreads();
;         {
;             typedef short s16x4_t __attribute__((ext_vector_type(4)));
;             const int ln = tid & 63, wq = tid >> 6, li = ln & 15, gq = li >> 2, gp = li & 3, G4 = ln >> 4;
; #pragma unroll
;             for (int i = 0; i < 4; ++i) {
;                 const int nb = wq, k8 = 2 * (G4 + 4 * (i >> 1)) + (i & 1);
;                 const LAS unsigned char* p0 = lds + (8 * k8 + gq) * RS + (16 * nb + 4 * gp) * 2;
;                 const s16x4_t x0 = __builtin_amdgcn_ds_read_tr16_b64_v4i16((LAS s16x4_t*)p0), x1 = __builtin_amdgcn_ds_read_tr16_b64_v4i16((LAS s16x4_t*)(p0 + 4 * RS));
;                 typedef short s16x8_t __attribute__((ext_vector_type(8)));
;                 const s16x8_t o8 = (s16x8_t){x0[0], x0[1], x0[2], x0[3], x1[0], x1[1], x1[2], x1[3]};
;                 *(u32x4*)(dst + (size_t)(16 * nb + li) * K + k8 * 8) = __builtin_bit_cast(u32x4, o8);
;             }
;         }
;         __syncthreads();
;         t += step; src = srcn; dst = dstn; ld = ldn; K = Kn; srcn = srcm; dstn = dstm; ldn = ldm; Kn = Km;
.Lmy_cv1_1_668:
	s_waitcnt vmcnt(23)
	v_cvt_pk_bf16_f32 v60, v60, v61
	v_cvt_pk_bf16_f32 v61, v62, v63
	s_waitcnt vmcnt(22)
	v_cvt_pk_bf16_f32 v62, v56, v57
	v_cvt_pk_bf16_f32 v63, v58, v59
	ds_write2st64_b64 v116, v[60:61], v[62:63] offset1:10
	s_waitcnt vmcnt(21)
	v_cvt_pk_bf16_f32 v60, v52, v53
	v_cvt_pk_bf16_f32 v61, v54, v55
	s_waitcnt vmcnt(20)
	v_cvt_pk_bf16_f32 v62, v48, v49
	v_cvt_pk_bf16_f32 v63, v50, v51
	ds_write2st64_b64 v116, v[60:61], v[62:63] offset0:20 offset1:30
	s_waitcnt vmcnt(19)
	v_cvt_pk_bf16_f32 v60, v44, v45
	v_cvt_pk_bf16_f32 v61, v46, v47
	s_waitcnt vmcnt(18)
	v_cvt_pk_bf16_f32 v62, v40, v41
	v_cvt_pk_bf16_f32 v63, v42, v43
	ds_write2st64_b64 v116, v[60:61], v[62:63] offset0:40 offset1:50
	s_waitcnt vmcnt(17)
	v_cvt_pk_bf16_f32 v60, v36, v37
	v_cvt_pk_bf16_f32 v61, v38, v39
	s_waitcnt vmcnt(16)
	v_cvt_pk_bf16_f32 v62, v32, v33
	v_cvt_pk_bf16_f32 v63, v34, v35
	ds_write2st64_b64 v116, v[60:61], v[62:63] offset0:60 offset1:70
	v_mul_lo_u32 v62, s9, v114
	v_mul_lo_u32 v63, s8, v115
	v_mad_u64_u32 v[60:61], s[8:9], s8, v114, 0
	v_add3_u32 v61, v61, v63, v62
	s_waitcnt lgkmcnt(0)
	s_barrier
	v_lshl_add_u64 v[44:45], v[60:61], 1, s[6:7]
	ds_read_b64_tr_b16 v[60:61], v117
	ds_read_b64_tr_b16 v[62:63], v117 offset:1280
	ds_read_b64_tr_b16 v[56:57], v118
	ds_read_b64_tr_b16 v[58:59], v118 offset:1280
	ds_read_b64_tr_b16 v[52:53], v119
	ds_read_b64_tr_b16 v[54:55], v119 offset:1280
	ds_read_b64_tr_b16 v[48:49], v120
	ds_read_b64_tr_b16 v[50:51], v120 offset:1280
	v_lshl_add_u64 v[44:45], v[44:45], 0, v[162:163]
	s_waitcnt lgkmcnt(6)
	global_store_dwordx4 v[44:45], v[60:63], off
	s_waitcnt lgkmcnt(4)
	global_store_dwordx4 v[44:45], v[56:59], off offset:16
	s_waitcnt lgkmcnt(2)
	global_store_dwordx4 v[44:45], v[52:55], off offset:128
	s_waitcnt lgkmcnt(0)
	global_store_dwordx4 v[44:45], v[48:51], off offset:144
	s_add_i32 s18, s18, 1
	s_cmp_lt_i32 s18, s26
	s_mov_b64 s[8:9], s[24:25]
	s_mov_b64 s[6:7], s[22:23]
	s_barrier
	s_cbranch_scc0 .LBB0_671
.Lmy_cv1_2_669:
	s_mov_b64 s[24:25], s[4:5]
	s_add_i32 s4, s18, 2
	s_mov_b64 s[22:23], s[2:3]
	s_mov_b64 s[2:3], 0
	s_cmp_ge_i32 s4, s26
	s_mov_b64 s[4:5], 0
	s_cbranch_scc1 .Lmy_cv1_strict_2
	s_cmpk_lt_i32 s18, 0xffe
	s_cselect_b32 s2, 0x1000, s63
	s_add_i32 s27, s2, s18
	s_add_i32 s2, s27, 2
	s_ashr_i32 s3, s2, 31
	s_lshr_b32 s3, s3, 19
	s_add_i32 s3, s2, s3
	s_ashr_i32 s29, s3, 13
	s_and_b32 s3, s3, 0xe000
	s_sub_i32 s28, s2, s3
	s_sext_i32_i16 s2, s28
	s_bfe_u32 s2, s2, 0x70018
	s_add_i32 s30, s28, s2
	s_sext_i32_i16 s2, s30
	s_lshr_b32 s2, s2, 7
	s_bfe_i64 s[2:3], s[2:3], 0x100000
	s_lshl_b64 s[4:5], s[2:3], 23
	s_add_u32 s31, s60, s4
	s_addc_u32 s33, s61, s5
	s_and_b32 s2, s30, 0xff80
	s_sub_i32 s2, s28, s2
	s_bfe_i32 s3, s2, 0x80000
	s_bfe_u32 s3, s3, 0x3000c
	s_add_i32 s3, s2, s3
	s_bfe_i32 s28, s3, 0x80000
	s_and_b32 s3, s3, 0xf8
	s_sub_i32 s2, s2, s3
	s_sext_i32_i8 s30, s2
	s_lshl_b32 s2, s30, 8
	s_lshl_b32 s3, s29, 7
	s_add_i32 s2, s2, s3
	s_sext_i32_i16 s28, s28
	s_ashr_i32 s3, s2, 31
	s_lshr_b32 s28, s28, 3
	s_lshl_b64 s[2:3], s[2:3], 12
	s_add_u32 s29, s31, s2
	s_addc_u32 s31, s33, s3
	s_lshl_b32 s2, s28, 7
	s_ashr_i32 s3, s2, 31
	s_lshl_b64 s[2:3], s[2:3], 1
	s_add_u32 s2, s29, s2
	s_addc_u32 s3, s31, s3
	s_addk_i32 s27, 0x2001
	s_cmpk_lt_u32 s27, 0x3fff
	s_cselect_b32 s29, s58, s84
	s_cselect_b32 s27, s59, s85
	s_add_u32 s29, s29, s4
	s_addc_u32 s27, s27, s5
	s_bfe_i64 s[4:5], s[28:29], 0x100000
	s_lshl_b64 s[4:5], s[4:5], 19
	s_add_u32 s28, s29, s4
	s_addc_u32 s27, s27, s5
	s_lshl_b32 s4, s30, 7
	s_ashr_i32 s5, s4, 31
	s_lshl_b64 s[4:5], s[4:5], 2
	s_add_u32 s4, s28, s4
	s_addc_u32 s5, s27, s5
	v_mov_b32_e32 v113, v163
	v_lshl_add_u64 v[32:33], s[4:5], 0, v[112:113]
	v_lshl_add_u64 v[56:57], v[32:33], 0, v[96:97]
	v_lshl_add_u64 v[58:59], v[32:33], 0, v[98:99]
	v_lshl_add_u64 v[48:49], v[32:33], 0, v[100:101]
	v_lshl_add_u64 v[50:51], v[32:33], 0, v[102:103]
	v_lshl_add_u64 v[40:41], v[32:33], 0, v[104:105]
	v_lshl_add_u64 v[42:43], v[32:33], 0, v[106:107]
	v_lshl_add_u64 v[34:35], v[32:33], 0, v[108:109]
	v_lshl_add_u64 v[32:33], v[32:33], 0, v[110:111]
	global_load_dwordx4 v[60:63], v[56:57], off nt
	s_nop 0
	global_load_dwordx4 v[56:59], v[58:59], off nt
	s_nop 0
	global_load_dwordx4 v[52:55], v[48:49], off nt
	s_nop 0
	global_load_dwordx4 v[48:51], v[50:51], off nt
	s_nop 0
	global_load_dwordx4 v[44:47], v[40:41], off nt
	s_nop 0
	global_load_dwordx4 v[40:43], v[42:43], off nt
	s_nop 0
	global_load_dwordx4 v[36:39], v[34:35], off nt
	s_nop 0
	global_load_dwordx4 v[32:35], v[32:33], off nt
	s_mov_b64 s[4:5], 0x800
	s_branch .Lmy_cv1_2_668

; #define LAS __attribute__((address_space(3)))
; __device__ __forceinline__ unsigned cvt_pk_bf16(float lo, float hi) { const bf16x2_t r = __builtin_convertvector((f32x2_t){lo, hi}, bf16x2_t); return __builtin_bit_cast(unsigned, r); }
; __device__ __forceinline__ void cvt_range(const MkArgs& a, LAS unsigned char* lds, const int tid, const int first, const int step, const int end, const bool deferred) {
;     ...
;         for (int i = 0; i < 8; ++i) {
;             u32x2 p; p[0] = cvt_pk_bf16(v[i][0], v[i][1]); p[1] = cvt_pk_bf16(v[i][2], v[i][3]);
;             *(LAS u32x2*)(lds + (kk + 16 * i) * RS + c4 * 8) = p;
;         }
;         __syncthreads();
;         {
;             typedef short s16x4_t __attribute__((ext_vector_type(4)));
;             const int ln = tid & 63, wq = tid >> 6, li = ln & 15, gq = li >> 2, gp = li & 3, G4 = ln >> 4;
; #pragma unroll
;             for (int i = 0; i < 4; ++i) {
;                 const int nb = wq, k8 = 2 * (G4 + 4 * (i >> 1)) + (i & 1);
;                 const LAS unsigned char* p0 = lds + (8 * k8 + gq) * RS + (16 * nb + 4 * gp) * 2;
;                 const s16x4_t x0 = __builtin_amdgcn_ds_read_tr16_b64_v4i16((LAS s16x4_t*)p0), x1 = __builtin_amdgcn_ds_read_tr16_b64_v4i16((LAS s16x4_t*)(p0 + 4 * RS));
;                 typedef short s16x8_t __attribute__((ext_vector_type(8)));
;                 const s16x8_t o8 = (s16x8_t){x0[0], x0[1], x0[2], x0[3], x1[0], x1[1], x1[2], x1[3]};
;                 *(u32x4*)(dst + (size_t)(16 * nb + li) * K + k8 * 8) = __builtin_bit_cast(u32x4, o8);
;             }
;         }
;         __syncthreads();
;         t += step; src = srcn; dst = dstn; ld = ldn; K = Kn; srcn = srcm; dstn = dstm; ldn = ldm; Kn = Km;
.Lmy_cv1_2_668:
	s_waitcnt vmcnt(23)
	v_cvt_pk_bf16_f32 v68, v68, v69
	v_cvt_pk_bf16_f32 v69, v70, v71
	s_waitcnt vmcnt(22)
	v_cvt_pk_bf16_f32 v70, v64, v65
	v_cvt_pk_bf16_f32 v71, v66, v67
	ds_write2st64_b64 v116, v[68:69], v[70:71] offset1:10
	s_waitcnt vmcnt(21)
	v_cvt_pk_bf16_f32 v68, v76, v77
	v_cvt_pk_bf16_f32 v69, v78, v79
	s_waitcnt vmcnt(20)
	v_cvt_pk_bf16_f32 v70, v72, v73
	v_cvt_pk_bf16_f32 v71, v74, v75
	ds_write2st64_b64 v116, v[68:69], v[70:71] offset0:20 offset1:30
	s_waitcnt vmcnt(19)
	v_cvt_pk_bf16_f32 v68, v84, v85
	v_cvt_pk_bf16_f32 v69, v86, v87
	s_waitcnt vmcnt(18)
	v_cvt_pk_bf16_f32 v70, v80, v81
	v_cvt_pk_bf16_f32 v71, v82, v83
	ds_write2st64_b64 v116, v[68:69], v[70:71] offset0:40 offset1:50
	s_waitcnt vmcnt(17)
	v_cvt_pk_bf16_f32 v68, v92, v93
	v_cvt_pk_bf16_f32 v69, v94, v95
	s_waitcnt vmcnt(16)
	v_cvt_pk_bf16_f32 v70, v88, v89
	v_cvt_pk_bf16_f32 v71, v90, v91
	ds_write2st64_b64 v116, v[68:69], v[70:71] offset0:60 offset1:70
	v_mul_lo_u32 v70, s9, v114
	v_mul_lo_u32 v71, s8, v115
	v_mad_u64_u32 v[68:69], s[8:9], s8, v114, 0
	v_add3_u32 v69, v69, v71, v70
	s_waitcnt lgkmcnt(0)
	s_barrier
	v_lshl_add_u64 v[84:85], v[68:69], 1, s[6:7]
	ds_read_b64_tr_b16 v[68:69], v117
	ds_read_b64_tr_b16 v[70:71], v117 offset:1280
	ds_read_b64_tr_b16 v[64:65], v118
	ds_read_b64_tr_b16 v[66:67], v118 offset:1280
	ds_read_b64_tr_b16 v[76:77], v119
	ds_read_b64_tr_b16 v[78:79], v119 offset:1280
	ds_read_b64_tr_b16 v[72:73], v120
	ds_read_b64_tr_b16 v[74:75], v120 offset:1280
	v_lshl_add_u64 v[84:85], v[84:85], 0, v[162:163]
	s_waitcnt lgkmcnt(6)
	global_store_dwordx4 v[84:85], v[68:71], off
	s_waitcnt lgkmcnt(4)
	global_store_dwordx4 v[84:85], v[64:67], off offset:16
	s_waitcnt lgkmcnt(2)
	global_store_dwordx4 v[84:85], v[76:79], off offset:128
	s_waitcnt lgkmcnt(0)
	global_store_dwordx4 v[84:85], v[72:75], off offset:144
	s_add_i32 s18, s18, 1
	s_cmp_lt_i32 s18, s26
	s_mov_b64 s[8:9], s[24:25]
	s_mov_b64 s[6:7], s[22:23]
	s_barrier
	s_cbranch_scc0 .LBB0_671

; #define LAS __attribute__((address_space(3)))
; __device__ __forceinline__ unsigned cvt_pk_bf16(float lo, float hi) { const bf16x2_t r = __builtin_convertvector((f32x2_t){lo, hi}, bf16x2_t); return __builtin_bit_cast(unsigned, r); }
; __device__ __forceinline__ void cvt_range(const MkArgs& a, LAS unsigned char* lds, const int tid, const int first, const int step, const int end, const bool deferred) {
;     ...
;         for (int i = 0; i < 8; ++i) {
;             u32x2 p; p[0] = cvt_pk_bf16(v[i][0], v[i][1]); p[1] = cvt_pk_bf16(v[i][2], v[i][3]);
;             *(LAS u32x2*)(lds + (kk + 16 * i) * RS + c4 * 8) = p;
;         }
;         __syncthreads();
;         {
;             typedef short s16x4_t __attribute__((ext_vector_type(4)));
;             const int ln = tid & 63, wq = tid >> 6, li = ln & 15, gq = li >> 2, gp = li & 3, G4 = ln >> 4;
; #pragma unroll
;             for (int i = 0; i < 4; ++i) {
;                 const int nb = wq, k8 = 2 * (G4 + 4 * (i >> 1)) + (i & 1);
;                 const LAS unsigned char* p0 = lds + (8 * k8 + gq) * RS + (16 * nb + 4 * gp) * 2;
;                 const s16x4_t x0 = __builtin_amdgcn_ds_read_tr16_b64_v4i16((LAS s16x4_t*)p0), x1 = __builtin_amdgcn_ds_read_tr16_b64_v4i16((LAS s16x4_t*)(p0 + 4 * RS));
;                 typedef short s16x8_t __attribute__((ext_vector_type(8)));
;                 const s16x8_t o8 = (s16x8_t){x0[0], x0[1], x0[2], x0[3], x1[0], x1[1], x1[2], x1[3]};
;                 *(u32x4*)(dst + (size_t)(16 * nb + li) * K + k8 * 8) = __builtin_bit_cast(u32x4, o8);
;             }
;         }
;         __syncthreads();
;         t += step; src = srcn; dst = dstn; ld = ldn; K = Kn; srcn = srcm; dstn = dstm; ldn = ldm; Kn = Km;
; #pragma unroll
;         for (int i = 0; i < 8; ++i) { v[i] = vn[i]; vn[i] = vm[i]; }
.LBB0_1064:
	s_waitcnt vmcnt(23)
	v_cvt_pk_bf16_f32 v0, v0, v1
	v_cvt_pk_bf16_f32 v1, v2, v3
	s_waitcnt vmcnt(22)
	v_cvt_pk_bf16_f32 v2, v4, v5
	v_cvt_pk_bf16_f32 v3, v6, v7
	ds_write2st64_b64 v118, v[0:1], v[2:3] offset1:10
	s_waitcnt vmcnt(21)
	v_cvt_pk_bf16_f32 v0, v8, v9
	v_cvt_pk_bf16_f32 v1, v10, v11
	s_waitcnt vmcnt(20)
	v_cvt_pk_bf16_f32 v2, v12, v13
	v_cvt_pk_bf16_f32 v3, v14, v15
	ds_write2st64_b64 v118, v[0:1], v[2:3] offset0:20 offset1:30
	s_waitcnt vmcnt(19)
	v_cvt_pk_bf16_f32 v0, v16, v17
	v_cvt_pk_bf16_f32 v1, v18, v19
	s_waitcnt vmcnt(18)
	v_cvt_pk_bf16_f32 v2, v20, v21
	v_cvt_pk_bf16_f32 v3, v22, v23
	ds_write2st64_b64 v118, v[0:1], v[2:3] offset0:40 offset1:50
	s_waitcnt vmcnt(17)
	v_cvt_pk_bf16_f32 v0, v24, v25
	v_cvt_pk_bf16_f32 v1, v26, v27
	s_waitcnt vmcnt(16)
	v_cvt_pk_bf16_f32 v2, v28, v29
	v_cvt_pk_bf16_f32 v3, v30, v31
	ds_write2st64_b64 v118, v[0:1], v[2:3] offset0:60 offset1:70
	v_mul_lo_u32 v2, s11, v114
	v_mul_lo_u32 v3, s10, v115
	v_mad_u64_u32 v[0:1], s[10:11], s10, v114, 0
	v_add3_u32 v1, v1, v3, v2
	s_waitcnt lgkmcnt(0)
	s_barrier
	v_lshl_add_u64 v[16:17], v[0:1], 1, s[8:9]
	ds_read_b64_tr_b16 v[0:1], v119
	ds_read_b64_tr_b16 v[2:3], v119 offset:1280
	ds_read_b64_tr_b16 v[4:5], v120
	ds_read_b64_tr_b16 v[6:7], v120 offset:1280
	ds_read_b64_tr_b16 v[8:9], v121
	ds_read_b64_tr_b16 v[10:11], v121 offset:1280
	ds_read_b64_tr_b16 v[12:13], v122
	ds_read_b64_tr_b16 v[14:15], v122 offset:1280
	v_mov_b32_e32 v117, v99
	v_lshl_add_u64 v[16:17], v[16:17], 0, v[116:117]
	s_waitcnt lgkmcnt(6)
	global_store_dwordx4 v[16:17], v[0:3], off
	s_waitcnt lgkmcnt(4)
	global_store_dwordx4 v[16:17], v[4:7], off offset:16
	s_waitcnt lgkmcnt(2)
	global_store_dwordx4 v[16:17], v[8:11], off offset:128
	s_waitcnt lgkmcnt(0)
	global_store_dwordx4 v[16:17], v[12:15], off offset:144
	s_add_i32 s36, s36, 1
	s_cmp_ge_i32 s36, s37
	s_mov_b64 s[10:11], s[18:19]
	s_mov_b64 s[8:9], s[16:17]
	s_barrier
	s_cbranch_scc1 .LBB0_1029

; #define LAS __attribute__((address_space(3)))
; __device__ __forceinline__ unsigned cvt_pk_bf16(float lo, float hi) { const bf16x2_t r = __builtin_convertvector((f32x2_t){lo, hi}, bf16x2_t); return __builtin_bit_cast(unsigned, r); }
; __device__ __forceinline__ void cvt_range(const MkArgs& a, LAS unsigned char* lds, const int tid, const int first, const int step, const int end, const bool deferred) {
;     ...
;         if (tm < end) { cvt_decode(cvt_map(tm, deferred), w_in, w_out, w_eg, w_eu, w_ed, WinT, WoutT, WguT, WdT, srcm, dstm, ldm, Km);
; #pragma unroll
;             for (int i = 0; i < 8; ++i) vm[i] = __builtin_nontemporal_load((const f32x4*)(srcm + (size_t)(kk + 16 * i) * ldm + c4 * 4)); }
; #pragma unroll
;         for (int i = 0; i < 8; ++i) {
;             u32x2 p; p[0] = cvt_pk_bf16(v[i][0], v[i][1]); p[1] = cvt_pk_bf16(v[i][2], v[i][3]);
;             *(LAS u32x2*)(lds + (kk + 16 * i) * RS + c4 * 8) = p;
;         }
;         __syncthreads();
;         {
;             typedef short s16x4_t __attribute__((ext_vector_type(4)));
;             const int ln = tid & 63, wq = tid >> 6, li = ln & 15, gq = li >> 2, gp = li & 3, G4 = ln >> 4;
; #pragma unroll
;             for (int i = 0; i < 4; ++i) {
;                 const int nb = wq, k8 = 2 * (G4 + 4 * (i >> 1)) + (i & 1);
;                 const LAS unsigned char* p0 = lds + (8 * k8 + gq) * RS + (16 * nb + 4 * gp) * 2;
;                 const s16x4_t x0 = __builtin_amdgcn_ds_read_tr16_b64_v4i16((LAS s16x4_t*)p0), x1 = __builtin_amdgcn_ds_read_tr16_b64_v4i16((LAS s16x4_t*)(p0 + 4 * RS));
;                 typedef short s16x8_t __attribute__((ext_vector_type(8)));
;                 const s16x8_t o8 = (s16x8_t){x0[0], x0[1], x0[2], x0[3], x1[0], x1[1], x1[2], x1[3]};
;                 *(u32x4*)(dst + (size_t)(16 * nb + li) * K + k8 * 8) = __builtin_bit_cast(u32x4, o8);
;             }
;         }
;         __syncthreads();
;         t += step; src = srcn; dst = dstn; ld = ldn; K = Kn; srcn = srcm; dstn = dstm; ldn = ldm; Kn = Km;
.Lmy_cv2_1_1063:
	v_lshl_add_u64 v[24:25], s[20:21], 0, v[98:99]
	v_mul_lo_u32 v2, s23, v96
	v_mul_lo_u32 v3, s22, v97
	v_mad_u64_u32 v[0:1], s[20:21], s22, v96, 0
	v_mul_lo_u32 v10, s23, v102
	v_mul_lo_u32 v11, s22, v103
	v_mad_u64_u32 v[8:9], s[20:21], s22, v102, 0
	v_mul_lo_u32 v18, s23, v106
	v_mul_lo_u32 v19, s22, v107
	v_mad_u64_u32 v[16:17], s[20:21], s22, v106, 0
	v_mul_lo_u32 v28, s23, v110
	v_mul_lo_u32 v29, s22, v111
	v_mad_u64_u32 v[26:27], s[20:21], s22, v110, 0
	v_add3_u32 v1, v1, v3, v2
	v_mul_lo_u32 v4, s23, v100
	v_mul_lo_u32 v5, s22, v101
	v_mad_u64_u32 v[2:3], s[20:21], s22, v100, 0
	v_add3_u32 v9, v9, v11, v10
	v_mul_lo_u32 v12, s23, v104
	v_mul_lo_u32 v13, s22, v105
	v_mad_u64_u32 v[10:11], s[20:21], s22, v104, 0
	v_add3_u32 v17, v17, v19, v18
	v_mul_lo_u32 v20, s23, v108
	v_mul_lo_u32 v21, s22, v109
	v_mad_u64_u32 v[18:19], s[20:21], s22, v108, 0
	v_add3_u32 v27, v27, v29, v28
	v_mul_lo_u32 v30, s23, v112
	v_mul_lo_u32 v31, s22, v113
	v_mad_u64_u32 v[28:29], s[20:21], s22, v112, 0
	v_add3_u32 v3, v3, v5, v4
	v_add3_u32 v11, v11, v13, v12
	v_add3_u32 v19, v19, v21, v20
	v_add3_u32 v29, v29, v31, v30
	v_lshl_add_u64 v[0:1], v[0:1], 2, v[24:25]
	v_lshl_add_u64 v[4:5], v[2:3], 2, v[24:25]
	v_lshl_add_u64 v[8:9], v[8:9], 2, v[24:25]
	v_lshl_add_u64 v[12:13], v[10:11], 2, v[24:25]
	v_lshl_add_u64 v[16:17], v[16:17], 2, v[24:25]
	v_lshl_add_u64 v[20:21], v[18:19], 2, v[24:25]
	v_lshl_add_u64 v[26:27], v[26:27], 2, v[24:25]
	v_lshl_add_u64 v[28:29], v[28:29], 2, v[24:25]
	global_load_dwordx4 v[0:3], v[0:1], off nt
	s_nop 0
	global_load_dwordx4 v[4:7], v[4:5], off nt
	s_nop 0
	global_load_dwordx4 v[8:11], v[8:9], off nt
	s_nop 0
	global_load_dwordx4 v[12:15], v[12:13], off nt
	s_nop 0
	global_load_dwordx4 v[16:19], v[16:17], off nt
	s_nop 0
	global_load_dwordx4 v[20:23], v[20:21], off nt
	s_nop 0
	global_load_dwordx4 v[24:27], v[26:27], off nt
	s_nop 0
	global_load_dwordx4 v[28:31], v[28:29], off nt
.Lmy_cv2_1_1064:
	s_waitcnt vmcnt(23)
	v_cvt_pk_bf16_f32 v36, v36, v37
	v_cvt_pk_bf16_f32 v37, v38, v39
	s_waitcnt vmcnt(22)
	v_cvt_pk_bf16_f32 v38, v32, v33
	v_cvt_pk_bf16_f32 v39, v34, v35
	ds_write2st64_b64 v118, v[36:37], v[38:39] offset1:10
	s_waitcnt vmcnt(21)
	v_cvt_pk_bf16_f32 v36, v44, v45
	v_cvt_pk_bf16_f32 v37, v46, v47
	s_waitcnt vmcnt(20)
	v_cvt_pk_bf16_f32 v38, v40, v41
	v_cvt_pk_bf16_f32 v39, v42, v43
	ds_write2st64_b64 v118, v[36:37], v[38:39] offset0:20 offset1:30
	s_waitcnt vmcnt(19)
	v_cvt_pk_bf16_f32 v36, v52, v53
	v_cvt_pk_bf16_f32 v37, v54, v55
	s_waitcnt vmcnt(18)
	v_cvt_pk_bf16_f32 v38, v48, v49
	v_cvt_pk_bf16_f32 v39, v50, v51
	ds_write2st64_b64 v118, v[36:37], v[38:39] offset0:40 offset1:50
	s_waitcnt vmcnt(17)
	v_cvt_pk_bf16_f32 v36, v60, v61
	v_cvt_pk_bf16_f32 v37, v62, v63
	s_waitcnt vmcnt(16)
	v_cvt_pk_bf16_f32 v38, v56, v57
	v_cvt_pk_bf16_f32 v39, v58, v59
	ds_write2st64_b64 v118, v[36:37], v[38:39] offset0:60 offset1:70
	v_mul_lo_u32 v38, s11, v114
	v_mul_lo_u32 v39, s10, v115
	v_mad_u64_u32 v[36:37], s[10:11], s10, v114, 0
	v_add3_u32 v37, v37, v39, v38
	s_waitcnt lgkmcnt(0)
	s_barrier
	v_lshl_add_u64 v[52:53], v[36:37], 1, s[8:9]
	ds_read_b64_tr_b16 v[36:37], v119
	ds_read_b64_tr_b16 v[38:39], v119 offset:1280
	ds_read_b64_tr_b16 v[32:33], v120
	ds_read_b64_tr_b16 v[34:35], v120 offset:1280
	ds_read_b64_tr_b16 v[44:45], v121
	ds_read_b64_tr_b16 v[46:47], v121 offset:1280
	ds_read_b64_tr_b16 v[40:41], v122
	ds_read_b64_tr_b16 v[42:43], v122 offset:1280
	v_mov_b32_e32 v117, v99
	v_lshl_add_u64 v[52:53], v[52:53], 0, v[116:117]
	s_waitcnt lgkmcnt(6)
	global_store_dwordx4 v[52:53], v[36:39], off
	s_waitcnt lgkmcnt(4)
	global_store_dwordx4 v[52:53], v[32:35], off offset:16
	s_waitcnt lgkmcnt(2)
	global_store_dwordx4 v[52:53], v[44:47], off offset:128
	s_waitcnt lgkmcnt(0)
	global_store_dwordx4 v[52:53], v[40:43], off offset:144
	s_add_i32 s36, s36, 1
	s_cmp_ge_i32 s36, s37
	s_mov_b64 s[10:11], s[18:19]
	s_mov_b64 s[8:9], s[16:17]
	s_barrier
	s_cbranch_scc1 .LBB0_1029

; #define LAS __attribute__((address_space(3)))
; __device__ __forceinline__ unsigned cvt_pk_bf16(float lo, float hi) { const bf16x2_t r = __builtin_convertvector((f32x2_t){lo, hi}, bf16x2_t); return __builtin_bit_cast(unsigned, r); }
; __device__ __forceinline__ void cvt_range(const MkArgs& a, LAS unsigned char* lds, const int tid, const int first, const int step, const int end, const bool deferred) {
;     ...
;         if (tm < end) { cvt_decode(cvt_map(tm, deferred), w_in, w_out, w_eg, w_eu, w_ed, WinT, WoutT, WguT, WdT, srcm, dstm, ldm, Km);
; #pragma unroll
;             for (int i = 0; i < 8; ++i) vm[i] = __builtin_nontemporal_load((const f32x4*)(srcm + (size_t)(kk + 16 * i) * ldm + c4 * 4)); }
; #pragma unroll
;         for (int i = 0; i < 8; ++i) {
;             u32x2 p; p[0] = cvt_pk_bf16(v[i][0], v[i][1]); p[1] = cvt_pk_bf16(v[i][2], v[i][3]);
;             *(LAS u32x2*)(lds + (kk + 16 * i) * RS + c4 * 8) = p;
;         }
;         __syncthreads();
;         {
;             typedef short s16x4_t __attribute__((ext_vector_type(4)));
;             const int ln = tid & 63, wq = tid >> 6, li = ln & 15, gq = li >> 2, gp = li & 3, G4 = ln >> 4;
; #pragma unroll
;             for (int i = 0; i < 4; ++i) {
;                 const int nb = wq, k8 = 2 * (G4 + 4 * (i >> 1)) + (i & 1);
;                 const LAS unsigned char* p0 = lds + (8 * k8 + gq) * RS + (16 * nb + 4 * gp) * 2;
;                 const s16x4_t x0 = __builtin_amdgcn_ds_read_tr16_b64_v4i16((LAS s16x4_t*)p0), x1 = __builtin_amdgcn_ds_read_tr16_b64_v4i16((LAS s16x4_t*)(p0 + 4 * RS));
;                 typedef short s16x8_t __attribute__((ext_vector_type(8)));
;                 const s16x8_t o8 = (s16x8_t){x0[0], x0[1], x0[2], x0[3], x1[0], x1[1], x1[2], x1[3]};
;                 *(u32x4*)(dst + (size_t)(16 * nb + li) * K + k8 * 8) = __builtin_bit_cast(u32x4, o8);
;             }
;         }
;         __syncthreads();
;         t += step; src = srcn; dst = dstn; ld = ldn; K = Kn; srcn = srcm; dstn = dstm; ldn = ldm; Kn = Km;
.Lmy_cv2_2_1063:
	v_lshl_add_u64 v[60:61], s[20:21], 0, v[98:99]
	v_mul_lo_u32 v38, s23, v96
	v_mul_lo_u32 v39, s22, v97
	v_mad_u64_u32 v[36:37], s[20:21], s22, v96, 0
	v_mul_lo_u32 v46, s23, v102
	v_mul_lo_u32 v47, s22, v103
	v_mad_u64_u32 v[44:45], s[20:21], s22, v102, 0
	v_mul_lo_u32 v54, s23, v106
	v_mul_lo_u32 v55, s22, v107
	v_mad_u64_u32 v[52:53], s[20:21], s22, v106, 0
	v_mul_lo_u32 v56, s23, v110
	v_mul_lo_u32 v57, s22, v111
	v_mad_u64_u32 v[62:63], s[20:21], s22, v110, 0
	v_add3_u32 v37, v37, v39, v38
	v_mul_lo_u32 v32, s23, v100
	v_mul_lo_u32 v33, s22, v101
	v_mad_u64_u32 v[38:39], s[20:21], s22, v100, 0
	v_add3_u32 v45, v45, v47, v46
	v_mul_lo_u32 v40, s23, v104
	v_mul_lo_u32 v41, s22, v105
	v_mad_u64_u32 v[46:47], s[20:21], s22, v104, 0
	v_add3_u32 v53, v53, v55, v54
	v_mul_lo_u32 v48, s23, v108
	v_mul_lo_u32 v49, s22, v109
	v_mad_u64_u32 v[54:55], s[20:21], s22, v108, 0
	v_add3_u32 v63, v63, v57, v56
	v_mul_lo_u32 v58, s23, v112
	v_mul_lo_u32 v59, s22, v113
	v_mad_u64_u32 v[56:57], s[20:21], s22, v112, 0
	v_add3_u32 v39, v39, v33, v32
	v_add3_u32 v47, v47, v41, v40
	v_add3_u32 v55, v55, v49, v48
	v_add3_u32 v57, v57, v59, v58
	v_lshl_add_u64 v[36:37], v[36:37], 2, v[60:61]
	v_lshl_add_u64 v[32:33], v[38:39], 2, v[60:61]
	v_lshl_add_u64 v[44:45], v[44:45], 2, v[60:61]
	v_lshl_add_u64 v[40:41], v[46:47], 2, v[60:61]
	v_lshl_add_u64 v[52:53], v[52:53], 2, v[60:61]
	v_lshl_add_u64 v[48:49], v[54:55], 2, v[60:61]
	v_lshl_add_u64 v[62:63], v[62:63], 2, v[60:61]
	v_lshl_add_u64 v[56:57], v[56:57], 2, v[60:61]
	global_load_dwordx4 v[36:39], v[36:37], off nt
	s_nop 0
	global_load_dwordx4 v[32:35], v[32:33], off nt
	s_nop 0
	global_load_dwordx4 v[44:47], v[44:45], off nt
	s_nop 0
	global_load_dwordx4 v[40:43], v[40:41], off nt
	s_nop 0
	global_load_dwordx4 v[52:55], v[52:53], off nt
	s_nop 0
	global_load_dwordx4 v[48:51], v[48:49], off nt
	s_nop 0
	global_load_dwordx4 v[60:63], v[62:63], off nt
	s_nop 0
	global_load_dwordx4 v[56:59], v[56:57], off nt
.Lmy_cv2_2_1064:
	s_waitcnt vmcnt(23)
	v_cvt_pk_bf16_f32 v64, v64, v65
	v_cvt_pk_bf16_f32 v65, v66, v67
	s_waitcnt vmcnt(22)
	v_cvt_pk_bf16_f32 v66, v68, v69
	v_cvt_pk_bf16_f32 v67, v70, v71
	ds_write2st64_b64 v118, v[64:65], v[66:67] offset1:10
	s_waitcnt vmcnt(21)
	v_cvt_pk_bf16_f32 v64, v72, v73
	v_cvt_pk_bf16_f32 v65, v74, v75
	s_waitcnt vmcnt(20)
	v_cvt_pk_bf16_f32 v66, v76, v77
	v_cvt_pk_bf16_f32 v67, v78, v79
	ds_write2st64_b64 v118, v[64:65], v[66:67] offset0:20 offset1:30
	s_waitcnt vmcnt(19)
	v_cvt_pk_bf16_f32 v64, v80, v81
	v_cvt_pk_bf16_f32 v65, v82, v83
	s_waitcnt vmcnt(18)
	v_cvt_pk_bf16_f32 v66, v84, v85
	v_cvt_pk_bf16_f32 v67, v86, v87
	ds_write2st64_b64 v118, v[64:65], v[66:67] offset0:40 offset1:50
	s_waitcnt vmcnt(17)
	v_cvt_pk_bf16_f32 v64, v88, v89
	v_cvt_pk_bf16_f32 v65, v90, v91
	s_waitcnt vmcnt(16)
	v_cvt_pk_bf16_f32 v66, v92, v93
	v_cvt_pk_bf16_f32 v67, v94, v95
	ds_write2st64_b64 v118, v[64:65], v[66:67] offset0:60 offset1:70
	v_mul_lo_u32 v66, s11, v114
	v_mul_lo_u32 v67, s10, v115
	v_mad_u64_u32 v[64:65], s[10:11], s10, v114, 0
	v_add3_u32 v65, v65, v67, v66
	s_waitcnt lgkmcnt(0)
	s_barrier
	v_lshl_add_u64 v[80:81], v[64:65], 1, s[8:9]
	ds_read_b64_tr_b16 v[64:65], v119
	ds_read_b64_tr_b16 v[66:67], v119 offset:1280
	ds_read_b64_tr_b16 v[68:69], v120
	ds_read_b64_tr_b16 v[70:71], v120 offset:1280
	ds_read_b64_tr_b16 v[72:73], v121
	ds_read_b64_tr_b16 v[74:75], v121 offset:1280
	ds_read_b64_tr_b16 v[76:77], v122
	ds_read_b64_tr_b16 v[78:79], v122 offset:1280
	v_mov_b32_e32 v117, v99
	v_lshl_add_u64 v[80:81], v[80:81], 0, v[116:117]
	s_waitcnt lgkmcnt(6)
	global_store_dwordx4 v[80:81], v[64:67], off
	s_waitcnt lgkmcnt(4)
	global_store_dwordx4 v[80:81], v[68:71], off offset:16
	s_waitcnt lgkmcnt(2)
	global_store_dwordx4 v[80:81], v[72:75], off offset:128
	s_waitcnt lgkmcnt(0)
	global_store_dwordx4 v[80:81], v[76:79], off offset:144
	s_add_i32 s36, s36, 1
	s_cmp_ge_i32 s36, s37
	s_mov_b64 s[10:11], s[18:19]
	s_mov_b64 s[8:9], s[16:17]
	s_barrier
	s_cbranch_scc1 .LBB0_1029

; #define LAS __attribute__((address_space(3)))
; __device__ __forceinline__ unsigned cvt_pk_bf16(float lo, float hi) { const bf16x2_t r = __builtin_convertvector((f32x2_t){lo, hi}, bf16x2_t); return __builtin_bit_cast(unsigned, r); }
; __device__ __forceinline__ void cvt_range(const MkArgs& a, LAS unsigned char* lds, const int tid, const int first, const int step, const int end, const bool deferred) {
;     ...
;         for (int i = 0; i < 8; ++i) {
;             u32x2 p; p[0] = cvt_pk_bf16(v[i][0], v[i][1]); p[1] = cvt_pk_bf16(v[i][2], v[i][3]);
;             *(LAS u32x2*)(lds + (kk + 16 * i) * RS + c4 * 8) = p;
;         }
;         __syncthreads();
;         {
;             typedef short s16x4_t __attribute__((ext_vector_type(4)));
;             const int ln = tid & 63, wq = tid >> 6, li = ln & 15, gq = li >> 2, gp = li & 3, G4 = ln >> 4;
; #pragma unroll
;             for (int i = 0; i < 4; ++i) {
;                 const int nb = wq, k8 = 2 * (G4 + 4 * (i >> 1)) + (i & 1);
;                 const LAS unsigned char* p0 = lds + (8 * k8 + gq) * RS + (16 * nb + 4 * gp) * 2;
;                 const s16x4_t x0 = __builtin_amdgcn_ds_read_tr16_b64_v4i16((LAS s16x4_t*)p0), x1 = __builtin_amdgcn_ds_read_tr16_b64_v4i16((LAS s16x4_t*)(p0 + 4 * RS));
;                 typedef short s16x8_t __attribute__((ext_vector_type(8)));
;                 const s16x8_t o8 = (s16x8_t){x0[0], x0[1], x0[2], x0[3], x1[0], x1[1], x1[2], x1[3]};
;                 *(u32x4*)(dst + (size_t)(16 * nb + li) * K + k8 * 8) = __builtin_bit_cast(u32x4, o8);
;             }
;         }
;         __syncthreads();
;         t += step; src = srcn; dst = dstn; ld = ldn; K = Kn; srcn = srcm; dstn = dstm; ldn = ldm; Kn = Km;
; #pragma unroll
;         for (int i = 0; i < 8; ++i) { v[i] = vn[i]; vn[i] = vm[i]; }
.LBB0_1234:
	s_waitcnt vmcnt(23)
	v_cvt_pk_bf16_f32 v0, v0, v1
	v_cvt_pk_bf16_f32 v1, v2, v3
	s_waitcnt vmcnt(22)
	v_cvt_pk_bf16_f32 v2, v4, v5
	v_cvt_pk_bf16_f32 v3, v6, v7
	ds_write2st64_b64 v118, v[0:1], v[2:3] offset1:10
	s_waitcnt vmcnt(21)
	v_cvt_pk_bf16_f32 v0, v8, v9
	v_cvt_pk_bf16_f32 v1, v10, v11
	s_waitcnt vmcnt(20)
	v_cvt_pk_bf16_f32 v2, v12, v13
	v_cvt_pk_bf16_f32 v3, v14, v15
	ds_write2st64_b64 v118, v[0:1], v[2:3] offset0:20 offset1:30
	s_waitcnt vmcnt(19)
	v_cvt_pk_bf16_f32 v0, v16, v17
	v_cvt_pk_bf16_f32 v1, v18, v19
	s_waitcnt vmcnt(18)
	v_cvt_pk_bf16_f32 v2, v20, v21
	v_cvt_pk_bf16_f32 v3, v22, v23
	ds_write2st64_b64 v118, v[0:1], v[2:3] offset0:40 offset1:50
	s_waitcnt vmcnt(17)
	v_cvt_pk_bf16_f32 v0, v24, v25
	v_cvt_pk_bf16_f32 v1, v26, v27
	s_waitcnt vmcnt(16)
	v_cvt_pk_bf16_f32 v2, v28, v29
	v_cvt_pk_bf16_f32 v3, v30, v31
	ds_write2st64_b64 v118, v[0:1], v[2:3] offset0:60 offset1:70
	v_mul_lo_u32 v2, s11, v114
	v_mul_lo_u32 v3, s10, v115
	v_mad_u64_u32 v[0:1], s[10:11], s10, v114, 0
	v_add3_u32 v1, v1, v3, v2
	s_waitcnt lgkmcnt(0)
	s_barrier
	v_lshl_add_u64 v[16:17], v[0:1], 1, s[8:9]
	ds_read_b64_tr_b16 v[0:1], v119
	ds_read_b64_tr_b16 v[2:3], v119 offset:1280
	ds_read_b64_tr_b16 v[4:5], v120
	ds_read_b64_tr_b16 v[6:7], v120 offset:1280
	ds_read_b64_tr_b16 v[8:9], v121
	ds_read_b64_tr_b16 v[10:11], v121 offset:1280
	ds_read_b64_tr_b16 v[12:13], v122
	ds_read_b64_tr_b16 v[14:15], v122 offset:1280
	v_mov_b32_e32 v117, v99
	v_lshl_add_u64 v[16:17], v[16:17], 0, v[116:117]
	s_waitcnt lgkmcnt(6)
	global_store_dwordx4 v[16:17], v[0:3], off
	s_waitcnt lgkmcnt(4)
	global_store_dwordx4 v[16:17], v[4:7], off offset:16
	s_waitcnt lgkmcnt(2)
	global_store_dwordx4 v[16:17], v[8:11], off offset:128
	s_waitcnt lgkmcnt(0)
	global_store_dwordx4 v[16:17], v[12:15], off offset:144
	s_add_i32 s38, s38, 1
	s_cmp_ge_i32 s38, s39
	s_mov_b64 s[10:11], s[18:19]
	s_mov_b64 s[8:9], s[16:17]
	s_barrier
	s_cbranch_scc1 .LBB0_1191

; #define LAS __attribute__((address_space(3)))
; __device__ __forceinline__ unsigned cvt_pk_bf16(float lo, float hi) { const bf16x2_t r = __builtin_convertvector((f32x2_t){lo, hi}, bf16x2_t); return __builtin_bit_cast(unsigned, r); }
; __device__ __forceinline__ void cvt_range(const MkArgs& a, LAS unsigned char* lds, const int tid, const int first, const int step, const int end, const bool deferred) {
;     ...
;     while (t < end) {
;         const int tm = t + 2 * step; const float* srcm = nullptr; bf16_t* dstm = nullptr; int ldm = 0, Km = 0;
;         if (tm < end) { cvt_decode(cvt_map(tm, deferred), w_in, w_out, w_eg, w_eu, w_ed, WinT, WoutT, WguT, WdT, srcm, dstm, ldm, Km);
; #pragma unroll
;             for (int i = 0; i < 8; ++i) vm[i] = __builtin_nontemporal_load((const f32x4*)(srcm + (size_t)(kk + 16 * i) * ldm + c4 * 4)); }
; #pragma unroll
;         for (int i = 0; i < 8; ++i) {
;             u32x2 p; p[0] = cvt_pk_bf16(v[i][0], v[i][1]); p[1] = cvt_pk_bf16(v[i][2], v[i][3]);
;             *(LAS u32x2*)(lds + (kk + 16 * i) * RS + c4 * 8) = p;
;         }
;         __syncthreads();
;         {
;             typedef short s16x4_t __attribute__((ext_vector_type(4)));
;             const int ln = tid & 63, wq = tid >> 6, li = ln & 15, gq = li >> 2, gp = li & 3, G4 = ln >> 4;
; #pragma unroll
;             for (int i = 0; i < 4; ++i) {
;                 const int nb = wq, k8 = 2 * (G4 + 4 * (i >> 1)) + (i & 1);
;                 const LAS unsigned char* p0 = lds + (8 * k8 + gq) * RS + (16 * nb + 4 * gp) * 2;
;                 const s16x4_t x0 = __builtin_amdgcn_ds_read_tr16_b64_v4i16((LAS s16x4_t*)p0), x1 = __builtin_amdgcn_ds_read_tr16_b64_v4i16((LAS s16x4_t*)(p0 + 4 * RS));
;                 typedef short s16x8_t __attribute__((ext_vector_type(8)));
;                 const s16x8_t o8 = (s16x8_t){x0[0], x0[1], x0[2], x0[3], x1[0], x1[1], x1[2], x1[3]};
;                 *(u32x4*)(dst + (size_t)(16 * nb + li) * K + k8 * 8) = __builtin_bit_cast(u32x4, o8);
;             }
;         }
;         __syncthreads();
;         t += step; src = srcn; dst = dstn; ld = ldn; K = Kn; srcn = srcm; dstn = dstm; ldn = ldm; Kn = Km;
; #pragma unroll
;         for (int i = 0; i < 8; ++i) { v[i] = vn[i]; vn[i] = vm[i]; }
;     }
.Lmy_cv3_1_1234:
	s_waitcnt vmcnt(23)
	v_cvt_pk_bf16_f32 v36, v36, v37
	v_cvt_pk_bf16_f32 v37, v38, v39
	s_waitcnt vmcnt(22)
	v_cvt_pk_bf16_f32 v38, v32, v33
	v_cvt_pk_bf16_f32 v39, v34, v35
	ds_write2st64_b64 v118, v[36:37], v[38:39] offset1:10
	s_waitcnt vmcnt(21)
	v_cvt_pk_bf16_f32 v36, v44, v45
	v_cvt_pk_bf16_f32 v37, v46, v47
	s_waitcnt vmcnt(20)
	v_cvt_pk_bf16_f32 v38, v40, v41
	v_cvt_pk_bf16_f32 v39, v42, v43
	ds_write2st64_b64 v118, v[36:37], v[38:39] offset0:20 offset1:30
	s_waitcnt vmcnt(19)
	v_cvt_pk_bf16_f32 v36, v52, v53
	v_cvt_pk_bf16_f32 v37, v54, v55
	s_waitcnt vmcnt(18)
	v_cvt_pk_bf16_f32 v38, v48, v49
	v_cvt_pk_bf16_f32 v39, v50, v51
	ds_write2st64_b64 v118, v[36:37], v[38:39] offset0:40 offset1:50
	s_waitcnt vmcnt(17)
	v_cvt_pk_bf16_f32 v36, v60, v61
	v_cvt_pk_bf16_f32 v37, v62, v63
	s_waitcnt vmcnt(16)
	v_cvt_pk_bf16_f32 v38, v56, v57
	v_cvt_pk_bf16_f32 v39, v58, v59
	ds_write2st64_b64 v118, v[36:37], v[38:39] offset0:60 offset1:70
	v_mul_lo_u32 v38, s11, v114
	v_mul_lo_u32 v39, s10, v115
	v_mad_u64_u32 v[36:37], s[10:11], s10, v114, 0
	v_add3_u32 v37, v37, v39, v38
	s_waitcnt lgkmcnt(0)
	s_barrier
	v_lshl_add_u64 v[52:53], v[36:37], 1, s[8:9]
	ds_read_b64_tr_b16 v[36:37], v119
	ds_read_b64_tr_b16 v[38:39], v119 offset:1280
	ds_read_b64_tr_b16 v[32:33], v120
	ds_read_b64_tr_b16 v[34:35], v120 offset:1280
	ds_read_b64_tr_b16 v[44:45], v121
	ds_read_b64_tr_b16 v[46:47], v121 offset:1280
	ds_read_b64_tr_b16 v[40:41], v122
	ds_read_b64_tr_b16 v[42:43], v122 offset:1280
	v_mov_b32_e32 v117, v99
	v_lshl_add_u64 v[52:53], v[52:53], 0, v[116:117]
	s_waitcnt lgkmcnt(6)
	global_store_dwordx4 v[52:53], v[36:39], off
	s_waitcnt lgkmcnt(4)
	global_store_dwordx4 v[52:53], v[32:35], off offset:16
	s_waitcnt lgkmcnt(2)
	global_store_dwordx4 v[52:53], v[44:47], off offset:128
	s_waitcnt lgkmcnt(0)
	global_store_dwordx4 v[52:53], v[40:43], off offset:144
	s_add_i32 s38, s38, 1
	s_cmp_ge_i32 s38, s39
	s_mov_b64 s[10:11], s[18:19]
	s_mov_b64 s[8:9], s[16:17]
	s_barrier
	s_cbranch_scc1 .LBB0_1191

; #define LAS __attribute__((address_space(3)))
; __device__ __forceinline__ unsigned cvt_pk_bf16(float lo, float hi) { const bf16x2_t r = __builtin_convertvector((f32x2_t){lo, hi}, bf16x2_t); return __builtin_bit_cast(unsigned, r); }
; __device__ __forceinline__ void cvt_range(const MkArgs& a, LAS unsigned char* lds, const int tid, const int first, const int step, const int end, const bool deferred) {
;     ...
;     while (t < end) {
;         const int tm = t + 2 * step; const float* srcm = nullptr; bf16_t* dstm = nullptr; int ldm = 0, Km = 0;
;         if (tm < end) { cvt_decode(cvt_map(tm, deferred), w_in, w_out, w_eg, w_eu, w_ed, WinT, WoutT, WguT, WdT, srcm, dstm, ldm, Km);
; #pragma unroll
;             for (int i = 0; i < 8; ++i) vm[i] = __builtin_nontemporal_load((const f32x4*)(srcm + (size_t)(kk + 16 * i) * ldm + c4 * 4)); }
; #pragma unroll
;         for (int i = 0; i < 8; ++i) {
;             u32x2 p; p[0] = cvt_pk_bf16(v[i][0], v[i][1]); p[1] = cvt_pk_bf16(v[i][2], v[i][3]);
;             *(LAS u32x2*)(lds + (kk + 16 * i) * RS + c4 * 8) = p;
;         }
;         __syncthreads();
;         {
;             typedef short s16x4_t __attribute__((ext_vector_type(4)));
;             const int ln = tid & 63, wq = tid >> 6, li = ln & 15, gq = li >> 2, gp = li & 3, G4 = ln >> 4;
; #pragma unroll
;             for (int i = 0; i < 4; ++i) {
;                 const int nb = wq, k8 = 2 * (G4 + 4 * (i >> 1)) + (i & 1);
;                 const LAS unsigned char* p0 = lds + (8 * k8 + gq) * RS + (16 * nb + 4 * gp) * 2;
;                 const s16x4_t x0 = __builtin_amdgcn_ds_read_tr16_b64_v4i16((LAS s16x4_t*)p0), x1 = __builtin_amdgcn_ds_read_tr16_b64_v4i16((LAS s16x4_t*)(p0 + 4 * RS));
;                 typedef short s16x8_t __attribute__((ext_vector_type(8)));
;                 const s16x8_t o8 = (s16x8_t){x0[0], x0[1], x0[2], x0[3], x1[0], x1[1], x1[2], x1[3]};
;                 *(u32x4*)(dst + (size_t)(16 * nb + li) * K + k8 * 8) = __builtin_bit_cast(u32x4, o8);
;             }
;         }
;         __syncthreads();
;         t += step; src = srcn; dst = dstn; ld = ldn; K = Kn; srcn = srcm; dstn = dstm; ldn = ldm; Kn = Km;
; #pragma unroll
;         for (int i = 0; i < 8; ++i) { v[i] = vn[i]; vn[i] = vm[i]; }
;     }
.Lmy_cv3_2_1234:
	s_waitcnt vmcnt(23)
	v_cvt_pk_bf16_f32 v64, v64, v65
	v_cvt_pk_bf16_f32 v65, v66, v67
	s_waitcnt vmcnt(22)
	v_cvt_pk_bf16_f32 v66, v68, v69
	v_cvt_pk_bf16_f32 v67, v70, v71
	ds_write2st64_b64 v118, v[64:65], v[66:67] offset1:10
	s_waitcnt vmcnt(21)
	v_cvt_pk_bf16_f32 v64, v72, v73
	v_cvt_pk_bf16_f32 v65, v74, v75
	s_waitcnt vmcnt(20)
	v_cvt_pk_bf16_f32 v66, v76, v77
	v_cvt_pk_bf16_f32 v67, v78, v79
	ds_write2st64_b64 v118, v[64:65], v[66:67] offset0:20 offset1:30
	s_waitcnt vmcnt(19)
	v_cvt_pk_bf16_f32 v64, v80, v81
	v_cvt_pk_bf16_f32 v65, v82, v83
	s_waitcnt vmcnt(18)
	v_cvt_pk_bf16_f32 v66, v84, v85
	v_cvt_pk_bf16_f32 v67, v86, v87
	ds_write2st64_b64 v118, v[64:65], v[66:67] offset0:40 offset1:50
	s_waitcnt vmcnt(17)
	v_cvt_pk_bf16_f32 v64, v88, v89
	v_cvt_pk_bf16_f32 v65, v90, v91
	s_waitcnt vmcnt(16)
	v_cvt_pk_bf16_f32 v66, v92, v93
	v_cvt_pk_bf16_f32 v67, v94, v95
	ds_write2st64_b64 v118, v[64:65], v[66:67] offset0:60 offset1:70
	v_mul_lo_u32 v66, s11, v114
	v_mul_lo_u32 v67, s10, v115
	v_mad_u64_u32 v[64:65], s[10:11], s10, v114, 0
	v_add3_u32 v65, v65, v67, v66
	s_waitcnt lgkmcnt(0)
	s_barrier
	v_lshl_add_u64 v[80:81], v[64:65], 1, s[8:9]
	ds_read_b64_tr_b16 v[64:65], v119
	ds_read_b64_tr_b16 v[66:67], v119 offset:1280
	ds_read_b64_tr_b16 v[68:69], v120
	ds_read_b64_tr_b16 v[70:71], v120 offset:1280
	ds_read_b64_tr_b16 v[72:73], v121
	ds_read_b64_tr_b16 v[74:75], v121 offset:1280
	ds_read_b64_tr_b16 v[76:77], v122
	ds_read_b64_tr_b16 v[78:79], v122 offset:1280
	v_mov_b32_e32 v117, v99
	v_lshl_add_u64 v[80:81], v[80:81], 0, v[116:117]
	s_waitcnt lgkmcnt(6)
	global_store_dwordx4 v[80:81], v[64:67], off
	s_waitcnt lgkmcnt(4)
	global_store_dwordx4 v[80:81], v[68:71], off offset:16
	s_waitcnt lgkmcnt(2)
	global_store_dwordx4 v[80:81], v[72:75], off offset:128
	s_waitcnt lgkmcnt(0)
	global_store_dwordx4 v[80:81], v[76:79], off offset:144
	s_add_i32 s38, s38, 1
	s_cmp_ge_i32 s38, s39
	s_mov_b64 s[10:11], s[18:19]
	s_mov_b64 s[8:9], s[16:17]
	s_barrier
	s_cbranch_scc1 .LBB0_1191

; #define LAS __attribute__((address_space(3)))
; __device__ __forceinline__ unsigned cvt_pk_bf16(float lo, float hi) { const bf16x2_t r = __builtin_convertvector((f32x2_t){lo, hi}, bf16x2_t); return __builtin_bit_cast(unsigned, r); }
; __device__ __forceinline__ void cvt_range(const MkArgs& a, LAS unsigned char* lds, const int tid, const int first, const int step, const int end, const bool deferred) {
;     ...
;         for (int i = 0; i < 8; ++i) {
;             u32x2 p; p[0] = cvt_pk_bf16(v[i][0], v[i][1]); p[1] = cvt_pk_bf16(v[i][2], v[i][3]);
;             *(LAS u32x2*)(lds + (kk + 16 * i) * RS + c4 * 8) = p;
;         }
;         __syncthreads();
;         {
;             typedef short s16x4_t __attribute__((ext_vector_type(4)));
;             const int ln = tid & 63, wq = tid >> 6, li = ln & 15, gq = li >> 2, gp = li & 3, G4 = ln >> 4;
; #pragma unroll
;             for (int i = 0; i < 4; ++i) {
;                 const int nb = wq, k8 = 2 * (G4 + 4 * (i >> 1)) + (i & 1);
;                 const LAS unsigned char* p0 = lds + (8 * k8 + gq) * RS + (16 * nb + 4 * gp) * 2;
;                 const s16x4_t x0 = __builtin_amdgcn_ds_read_tr16_b64_v4i16((LAS s16x4_t*)p0), x1 = __builtin_amdgcn_ds_read_tr16_b64_v4i16((LAS s16x4_t*)(p0 + 4 * RS));
;                 typedef short s16x8_t __attribute__((ext_vector_type(8)));
;                 const s16x8_t o8 = (s16x8_t){x0[0], x0[1], x0[2], x0[3], x1[0], x1[1], x1[2], x1[3]};
;                 *(u32x4*)(dst + (size_t)(16 * nb + li) * K + k8 * 8) = __builtin_bit_cast(u32x4, o8);
;             }
;         }
;         __syncthreads();
;         t += step; src = srcn; dst = dstn; ld = ldn; K = Kn; srcn = srcm; dstn = dstm; ldn = ldm; Kn = Km;
; #pragma unroll
;         for (int i = 0; i < 8; ++i) { v[i] = vn[i]; vn[i] = vm[i]; }
.LBB0_1737:
	s_waitcnt vmcnt(23)
	v_cvt_pk_bf16_f32 v0, v0, v1
	v_cvt_pk_bf16_f32 v1, v2, v3
	s_waitcnt vmcnt(22)
	v_cvt_pk_bf16_f32 v2, v4, v5
	v_cvt_pk_bf16_f32 v3, v6, v7
	ds_write2st64_b64 v109, v[0:1], v[2:3] offset1:10
	s_waitcnt vmcnt(21)
	v_cvt_pk_bf16_f32 v0, v8, v9
	v_cvt_pk_bf16_f32 v1, v10, v11
	s_waitcnt vmcnt(20)
	v_cvt_pk_bf16_f32 v2, v12, v13
	v_cvt_pk_bf16_f32 v3, v14, v15
	ds_write2st64_b64 v109, v[0:1], v[2:3] offset0:20 offset1:30
	s_waitcnt vmcnt(19)
	v_cvt_pk_bf16_f32 v0, v16, v17
	v_cvt_pk_bf16_f32 v1, v18, v19
	s_waitcnt vmcnt(18)
	v_cvt_pk_bf16_f32 v2, v20, v21
	v_cvt_pk_bf16_f32 v3, v22, v23
	ds_write2st64_b64 v109, v[0:1], v[2:3] offset0:40 offset1:50
	s_waitcnt vmcnt(17)
	v_cvt_pk_bf16_f32 v0, v24, v25
	v_cvt_pk_bf16_f32 v1, v26, v27
	s_waitcnt vmcnt(16)
	v_cvt_pk_bf16_f32 v2, v28, v29
	v_cvt_pk_bf16_f32 v3, v30, v31
	ds_write2st64_b64 v109, v[0:1], v[2:3] offset0:60 offset1:70
	v_mul_lo_u32 v2, s5, v96
	v_mul_lo_u32 v3, s4, v97
	v_mad_u64_u32 v[0:1], s[4:5], s4, v96, 0
	v_add3_u32 v1, v1, v3, v2
	s_waitcnt lgkmcnt(0)
	s_barrier
	v_lshl_add_u64 v[16:17], v[0:1], 1, s[2:3]
	ds_read_b64_tr_b16 v[0:1], v110
	ds_read_b64_tr_b16 v[2:3], v110 offset:1280
	ds_read_b64_tr_b16 v[4:5], v111
	ds_read_b64_tr_b16 v[6:7], v111 offset:1280
	ds_read_b64_tr_b16 v[8:9], v112
	ds_read_b64_tr_b16 v[10:11], v112 offset:1280
	ds_read_b64_tr_b16 v[12:13], v113
	ds_read_b64_tr_b16 v[14:15], v113 offset:1280
	v_mov_b32_e32 v99, v163
	v_lshl_add_u64 v[16:17], v[16:17], 0, v[98:99]
	s_waitcnt lgkmcnt(6)
	global_store_dwordx4 v[16:17], v[0:3], off
	s_waitcnt lgkmcnt(4)
	global_store_dwordx4 v[16:17], v[4:7], off offset:16
	s_waitcnt lgkmcnt(2)
	global_store_dwordx4 v[16:17], v[8:11], off offset:128
	s_waitcnt lgkmcnt(0)
	global_store_dwordx4 v[16:17], v[12:15], off offset:144
	s_add_i32 s30, s30, 1
	s_cmp_lt_i32 s30, s31
	s_mov_b64 s[4:5], s[24:25]
	s_mov_b64 s[2:3], s[22:23]
	s_barrier
	s_cbranch_scc0 .LBB0_1743

; #define LAS __attribute__((address_space(3)))
; __device__ __forceinline__ unsigned cvt_pk_bf16(float lo, float hi) { const bf16x2_t r = __builtin_convertvector((f32x2_t){lo, hi}, bf16x2_t); return __builtin_bit_cast(unsigned, r); }
; __device__ __forceinline__ void cvt_range(const MkArgs& a, LAS unsigned char* lds, const int tid, const int first, const int step, const int end, const bool deferred) {
;     ...
;         if (tm < end) { cvt_decode(cvt_map(tm, deferred), w_in, w_out, w_eg, w_eu, w_ed, WinT, WoutT, WguT, WdT, srcm, dstm, ldm, Km);
; #pragma unroll
;             for (int i = 0; i < 8; ++i) vm[i] = __builtin_nontemporal_load((const f32x4*)(srcm + (size_t)(kk + 16 * i) * ldm + c4 * 4)); }
; #pragma unroll
;         for (int i = 0; i < 8; ++i) {
;             u32x2 p; p[0] = cvt_pk_bf16(v[i][0], v[i][1]); p[1] = cvt_pk_bf16(v[i][2], v[i][3]);
;             *(LAS u32x2*)(lds + (kk + 16 * i) * RS + c4 * 8) = p;
;         }
;         __syncthreads();
;         {
;             typedef short s16x4_t __attribute__((ext_vector_type(4)));
;             const int ln = tid & 63, wq = tid >> 6, li = ln & 15, gq = li >> 2, gp = li & 3, G4 = ln >> 4;
; #pragma unroll
;             for (int i = 0; i < 4; ++i) {
;                 const int nb = wq, k8 = 2 * (G4 + 4 * (i >> 1)) + (i & 1);
;                 const LAS unsigned char* p0 = lds + (8 * k8 + gq) * RS + (16 * nb + 4 * gp) * 2;
;                 const s16x4_t x0 = __builtin_amdgcn_ds_read_tr16_b64_v4i16((LAS s16x4_t*)p0), x1 = __builtin_amdgcn_ds_read_tr16_b64_v4i16((LAS s16x4_t*)(p0 + 4 * RS));
;                 typedef short s16x8_t __attribute__((ext_vector_type(8)));
;                 const s16x8_t o8 = (s16x8_t){x0[0], x0[1], x0[2], x0[3], x1[0], x1[1], x1[2], x1[3]};
;                 *(u32x4*)(dst + (size_t)(16 * nb + li) * K + k8 * 8) = __builtin_bit_cast(u32x4, o8);
;             }
;         }
;         __syncthreads();
;         t += step; src = srcn; dst = dstn; ld = ldn; K = Kn; srcn = srcm; dstn = dstm; ldn = ldm; Kn = Km;
; #pragma unroll
;         for (int i = 0; i < 8; ++i) { v[i] = vn[i]; vn[i] = vm[i]; }
.Lmy_cv4_1_1736:
	v_lshlrev_b32_e32 v162, 2, v108
	v_lshl_add_u64 v[24:25], s[26:27], 0, v[162:163]
	v_mad_i64_i32 v[0:1], s[26:27], s28, v100, 0
	v_mad_i64_i32 v[2:3], s[26:27], s28, v101, 0
	v_mad_i64_i32 v[8:9], s[26:27], s28, v102, 0
	v_mad_i64_i32 v[10:11], s[26:27], s28, v103, 0
	v_mad_i64_i32 v[16:17], s[26:27], s28, v104, 0
	v_mad_i64_i32 v[18:19], s[26:27], s28, v105, 0
	v_mad_i64_i32 v[26:27], s[26:27], s28, v106, 0
	v_mad_i64_i32 v[28:29], s[26:27], s28, v107, 0
	v_lshl_add_u64 v[0:1], v[0:1], 2, v[24:25]
	v_lshl_add_u64 v[4:5], v[2:3], 2, v[24:25]
	v_lshl_add_u64 v[8:9], v[8:9], 2, v[24:25]
	v_lshl_add_u64 v[12:13], v[10:11], 2, v[24:25]
	v_lshl_add_u64 v[16:17], v[16:17], 2, v[24:25]
	v_lshl_add_u64 v[20:21], v[18:19], 2, v[24:25]
	v_lshl_add_u64 v[26:27], v[26:27], 2, v[24:25]
	v_lshl_add_u64 v[28:29], v[28:29], 2, v[24:25]
	global_load_dwordx4 v[0:3], v[0:1], off nt
	s_nop 0
	global_load_dwordx4 v[4:7], v[4:5], off nt
	s_nop 0
	global_load_dwordx4 v[8:11], v[8:9], off nt
	s_nop 0
	global_load_dwordx4 v[12:15], v[12:13], off nt
	s_nop 0
	global_load_dwordx4 v[16:19], v[16:17], off nt
	s_nop 0
	global_load_dwordx4 v[20:23], v[20:21], off nt
	s_nop 0
	global_load_dwordx4 v[24:27], v[26:27], off nt
	s_nop 0
	global_load_dwordx4 v[28:31], v[28:29], off nt
.Lmy_cv4_1_1737:
	s_waitcnt vmcnt(23)
	v_cvt_pk_bf16_f32 v36, v36, v37
	v_cvt_pk_bf16_f32 v37, v38, v39
	s_waitcnt vmcnt(22)
	v_cvt_pk_bf16_f32 v38, v32, v33
	v_cvt_pk_bf16_f32 v39, v34, v35
	ds_write2st64_b64 v109, v[36:37], v[38:39] offset1:10
	s_waitcnt vmcnt(21)
	v_cvt_pk_bf16_f32 v36, v44, v45
	v_cvt_pk_bf16_f32 v37, v46, v47
	s_waitcnt vmcnt(20)
	v_cvt_pk_bf16_f32 v38, v40, v41
	v_cvt_pk_bf16_f32 v39, v42, v43
	ds_write2st64_b64 v109, v[36:37], v[38:39] offset0:20 offset1:30
	s_waitcnt vmcnt(19)
	v_cvt_pk_bf16_f32 v36, v52, v53
	v_cvt_pk_bf16_f32 v37, v54, v55
	s_waitcnt vmcnt(18)
	v_cvt_pk_bf16_f32 v38, v48, v49
	v_cvt_pk_bf16_f32 v39, v50, v51
	ds_write2st64_b64 v109, v[36:37], v[38:39] offset0:40 offset1:50
	s_waitcnt vmcnt(17)
	v_cvt_pk_bf16_f32 v36, v60, v61
	v_cvt_pk_bf16_f32 v37, v62, v63
	s_waitcnt vmcnt(16)
	v_cvt_pk_bf16_f32 v38, v56, v57
	v_cvt_pk_bf16_f32 v39, v58, v59
	ds_write2st64_b64 v109, v[36:37], v[38:39] offset0:60 offset1:70
	v_mul_lo_u32 v38, s5, v96
	v_mul_lo_u32 v39, s4, v97
	v_mad_u64_u32 v[36:37], s[4:5], s4, v96, 0
	v_add3_u32 v37, v37, v39, v38
	s_waitcnt lgkmcnt(0)
	s_barrier
	v_lshl_add_u64 v[52:53], v[36:37], 1, s[2:3]
	ds_read_b64_tr_b16 v[36:37], v110
	ds_read_b64_tr_b16 v[38:39], v110 offset:1280
	ds_read_b64_tr_b16 v[32:33], v111
	ds_read_b64_tr_b16 v[34:35], v111 offset:1280
	ds_read_b64_tr_b16 v[44:45], v112
	ds_read_b64_tr_b16 v[46:47], v112 offset:1280
	ds_read_b64_tr_b16 v[40:41], v113
	ds_read_b64_tr_b16 v[42:43], v113 offset:1280
	v_mov_b32_e32 v99, v163
	v_lshl_add_u64 v[52:53], v[52:53], 0, v[98:99]
	s_waitcnt lgkmcnt(6)
	global_store_dwordx4 v[52:53], v[36:39], off
	s_waitcnt lgkmcnt(4)
	global_store_dwordx4 v[52:53], v[32:35], off offset:16
	s_waitcnt lgkmcnt(2)
	global_store_dwordx4 v[52:53], v[44:47], off offset:128
	s_waitcnt lgkmcnt(0)
	global_store_dwordx4 v[52:53], v[40:43], off offset:144
	s_add_i32 s30, s30, 1
	s_cmp_lt_i32 s30, s31
	s_mov_b64 s[4:5], s[24:25]
	s_mov_b64 s[2:3], s[22:23]
	s_barrier
	s_cbranch_scc0 .LBB0_1743

; #define LAS __attribute__((address_space(3)))
; __device__ __forceinline__ unsigned cvt_pk_bf16(float lo, float hi) { const bf16x2_t r = __builtin_convertvector((f32x2_t){lo, hi}, bf16x2_t); return __builtin_bit_cast(unsigned, r); }
; __device__ __forceinline__ void cvt_range(const MkArgs& a, LAS unsigned char* lds, const int tid, const int first, const int step, const int end, const bool deferred) {
;     ...
;         if (tm < end) { cvt_decode(cvt_map(tm, deferred), w_in, w_out, w_eg, w_eu, w_ed, WinT, WoutT, WguT, WdT, srcm, dstm, ldm, Km);
; #pragma unroll
;             for (int i = 0; i < 8; ++i) vm[i] = __builtin_nontemporal_load((const f32x4*)(srcm + (size_t)(kk + 16 * i) * ldm + c4 * 4)); }
; #pragma unroll
;         for (int i = 0; i < 8; ++i) {
;             u32x2 p; p[0] = cvt_pk_bf16(v[i][0], v[i][1]); p[1] = cvt_pk_bf16(v[i][2], v[i][3]);
;             *(LAS u32x2*)(lds + (kk + 16 * i) * RS + c4 * 8) = p;
;         }
;         __syncthreads();
;         {
;             typedef short s16x4_t __attribute__((ext_vector_type(4)));
;             const int ln = tid & 63, wq = tid >> 6, li = ln & 15, gq = li >> 2, gp = li & 3, G4 = ln >> 4;
; #pragma unroll
;             for (int i = 0; i < 4; ++i) {
;                 const int nb = wq, k8 = 2 * (G4 + 4 * (i >> 1)) + (i & 1);
;                 const LAS unsigned char* p0 = lds + (8 * k8 + gq) * RS + (16 * nb + 4 * gp) * 2;
;                 const s16x4_t x0 = __builtin_amdgcn_ds_read_tr16_b64_v4i16((LAS s16x4_t*)p0), x1 = __builtin_amdgcn_ds_read_tr16_b64_v4i16((LAS s16x4_t*)(p0 + 4 * RS));
;                 typedef short s16x8_t __attribute__((ext_vector_type(8)));
;                 const s16x8_t o8 = (s16x8_t){x0[0], x0[1], x0[2], x0[3], x1[0], x1[1], x1[2], x1[3]};
;                 *(u32x4*)(dst + (size_t)(16 * nb + li) * K + k8 * 8) = __builtin_bit_cast(u32x4, o8);
;             }
;         }
;         __syncthreads();
;         t += step; src = srcn; dst = dstn; ld = ldn; K = Kn; srcn = srcm; dstn = dstm; ldn = ldm; Kn = Km;
; #pragma unroll
;         for (int i = 0; i < 8; ++i) { v[i] = vn[i]; vn[i] = vm[i]; }
.Lmy_cv4_2_1736:
	v_lshlrev_b32_e32 v162, 2, v108
	v_lshl_add_u64 v[60:61], s[26:27], 0, v[162:163]
	v_mad_i64_i32 v[36:37], s[26:27], s28, v100, 0
	v_mad_i64_i32 v[38:39], s[26:27], s28, v101, 0
	v_mad_i64_i32 v[44:45], s[26:27], s28, v102, 0
	v_mad_i64_i32 v[46:47], s[26:27], s28, v103, 0
	v_mad_i64_i32 v[52:53], s[26:27], s28, v104, 0
	v_mad_i64_i32 v[54:55], s[26:27], s28, v105, 0
	v_mad_i64_i32 v[62:63], s[26:27], s28, v106, 0
	v_mad_i64_i32 v[56:57], s[26:27], s28, v107, 0
	v_lshl_add_u64 v[36:37], v[36:37], 2, v[60:61]
	v_lshl_add_u64 v[32:33], v[38:39], 2, v[60:61]
	v_lshl_add_u64 v[44:45], v[44:45], 2, v[60:61]
	v_lshl_add_u64 v[40:41], v[46:47], 2, v[60:61]
	v_lshl_add_u64 v[52:53], v[52:53], 2, v[60:61]
	v_lshl_add_u64 v[48:49], v[54:55], 2, v[60:61]
	v_lshl_add_u64 v[62:63], v[62:63], 2, v[60:61]
	v_lshl_add_u64 v[56:57], v[56:57], 2, v[60:61]
	global_load_dwordx4 v[36:39], v[36:37], off nt
	s_nop 0
	global_load_dwordx4 v[32:35], v[32:33], off nt
	s_nop 0
	global_load_dwordx4 v[44:47], v[44:45], off nt
	s_nop 0
	global_load_dwordx4 v[40:43], v[40:41], off nt
	s_nop 0
	global_load_dwordx4 v[52:55], v[52:53], off nt
	s_nop 0
	global_load_dwordx4 v[48:51], v[48:49], off nt
	s_nop 0
	global_load_dwordx4 v[60:63], v[62:63], off nt
	s_nop 0
	global_load_dwordx4 v[56:59], v[56:57], off nt
.Lmy_cv4_2_1737:
	s_waitcnt vmcnt(23)
	v_cvt_pk_bf16_f32 v64, v64, v65
	v_cvt_pk_bf16_f32 v65, v66, v67
	s_waitcnt vmcnt(22)
	v_cvt_pk_bf16_f32 v66, v68, v69
	v_cvt_pk_bf16_f32 v67, v70, v71
	ds_write2st64_b64 v109, v[64:65], v[66:67] offset1:10
	s_waitcnt vmcnt(21)
	v_cvt_pk_bf16_f32 v64, v72, v73
	v_cvt_pk_bf16_f32 v65, v74, v75
	s_waitcnt vmcnt(20)
	v_cvt_pk_bf16_f32 v66, v76, v77
	v_cvt_pk_bf16_f32 v67, v78, v79
	ds_write2st64_b64 v109, v[64:65], v[66:67] offset0:20 offset1:30
	s_waitcnt vmcnt(19)
	v_cvt_pk_bf16_f32 v64, v80, v81
	v_cvt_pk_bf16_f32 v65, v82, v83
	s_waitcnt vmcnt(18)
	v_cvt_pk_bf16_f32 v66, v84, v85
	v_cvt_pk_bf16_f32 v67, v86, v87
	ds_write2st64_b64 v109, v[64:65], v[66:67] offset0:40 offset1:50
	s_waitcnt vmcnt(17)
	v_cvt_pk_bf16_f32 v64, v88, v89
	v_cvt_pk_bf16_f32 v65, v90, v91
	s_waitcnt vmcnt(16)
	v_cvt_pk_bf16_f32 v66, v92, v93
	v_cvt_pk_bf16_f32 v67, v94, v95
	ds_write2st64_b64 v109, v[64:65], v[66:67] offset0:60 offset1:70
	v_mul_lo_u32 v66, s5, v96
	v_mul_lo_u32 v67, s4, v97
	v_mad_u64_u32 v[64:65], s[4:5], s4, v96, 0
	v_add3_u32 v65, v65, v67, v66
	s_waitcnt lgkmcnt(0)
	s_barrier
	v_lshl_add_u64 v[80:81], v[64:65], 1, s[2:3]
	ds_read_b64_tr_b16 v[64:65], v110
	ds_read_b64_tr_b16 v[66:67], v110 offset:1280
	ds_read_b64_tr_b16 v[68:69], v111
	ds_read_b64_tr_b16 v[70:71], v111 offset:1280
	ds_read_b64_tr_b16 v[72:73], v112
	ds_read_b64_tr_b16 v[74:75], v112 offset:1280
	ds_read_b64_tr_b16 v[76:77], v113
	ds_read_b64_tr_b16 v[78:79], v113 offset:1280
	v_mov_b32_e32 v99, v163
	v_lshl_add_u64 v[80:81], v[80:81], 0, v[98:99]
	s_waitcnt lgkmcnt(6)
	global_store_dwordx4 v[80:81], v[64:67], off
	s_waitcnt lgkmcnt(4)
	global_store_dwordx4 v[80:81], v[68:71], off offset:16
	s_waitcnt lgkmcnt(2)
	global_store_dwordx4 v[80:81], v[72:75], off offset:128
	s_waitcnt lgkmcnt(0)
	global_store_dwordx4 v[80:81], v[76:79], off offset:144
	s_add_i32 s30, s30, 1
	s_cmp_lt_i32 s30, s31
	s_mov_b64 s[4:5], s[24:25]
	s_mov_b64 s[2:3], s[22:23]
	s_barrier
	s_cbranch_scc0 .LBB0_1743

; #define LAS __attribute__((address_space(3)))
; __device__ __forceinline__ unsigned cvt_pk_bf16(float lo, float hi) { const bf16x2_t r = __builtin_convertvector((f32x2_t){lo, hi}, bf16x2_t); return __builtin_bit_cast(unsigned, r); }
; __device__ __forceinline__ void cvt_range(const MkArgs& a, LAS unsigned char* lds, const int tid, const int first, const int step, const int end, const bool deferred) {
;     ...
;         for (int i = 0; i < 8; ++i) {
;             u32x2 p; p[0] = cvt_pk_bf16(v[i][0], v[i][1]); p[1] = cvt_pk_bf16(v[i][2], v[i][3]);
;             *(LAS u32x2*)(lds + (kk + 16 * i) * RS + c4 * 8) = p;
;         }
;         __syncthreads();
;         {
;             typedef short s16x4_t __attribute__((ext_vector_type(4)));
;             const int ln = tid & 63, wq = tid >> 6, li = ln & 15, gq = li >> 2, gp = li & 3, G4 = ln >> 4;
; #pragma unroll
;             for (int i = 0; i < 4; ++i) {
;                 const int nb = wq, k8 = 2 * (G4 + 4 * (i >> 1)) + (i & 1);
;                 const LAS unsigned char* p0 = lds + (8 * k8 + gq) * RS + (16 * nb + 4 * gp) * 2;
;                 const s16x4_t x0 = __builtin_amdgcn_ds_read_tr16_b64_v4i16((LAS s16x4_t*)p0), x1 = __builtin_amdgcn_ds_read_tr16_b64_v4i16((LAS s16x4_t*)(p0 + 4 * RS));
;                 typedef short s16x8_t __attribute__((ext_vector_type(8)));
;                 const s16x8_t o8 = (s16x8_t){x0[0], x0[1], x0[2], x0[3], x1[0], x1[1], x1[2], x1[3]};
;                 *(u32x4*)(dst + (size_t)(16 * nb + li) * K + k8 * 8) = __builtin_bit_cast(u32x4, o8);
;             }
;         }
;         __syncthreads();
;         t += step; src = srcn; dst = dstn; ld = ldn; K = Kn; srcn = srcm; dstn = dstm; ldn = ldm; Kn = Km;
; #pragma unroll
;         for (int i = 0; i < 8; ++i) { v[i] = vn[i]; vn[i] = vm[i]; }
.LBB0_2123:
	s_waitcnt vmcnt(23)
	v_cvt_pk_bf16_f32 v0, v0, v1
	v_cvt_pk_bf16_f32 v1, v2, v3
	s_waitcnt vmcnt(22)
	v_cvt_pk_bf16_f32 v2, v4, v5
	v_cvt_pk_bf16_f32 v3, v6, v7
	ds_write2st64_b64 v101, v[0:1], v[2:3] offset1:10
	s_waitcnt vmcnt(21)
	v_cvt_pk_bf16_f32 v0, v8, v9
	v_cvt_pk_bf16_f32 v1, v10, v11
	s_waitcnt vmcnt(20)
	v_cvt_pk_bf16_f32 v2, v12, v13
	v_cvt_pk_bf16_f32 v3, v14, v15
	ds_write2st64_b64 v101, v[0:1], v[2:3] offset0:20 offset1:30
	s_waitcnt vmcnt(19)
	v_cvt_pk_bf16_f32 v0, v16, v17
	v_cvt_pk_bf16_f32 v1, v18, v19
	s_waitcnt vmcnt(18)
	v_cvt_pk_bf16_f32 v2, v20, v21
	v_cvt_pk_bf16_f32 v3, v22, v23
	ds_write2st64_b64 v101, v[0:1], v[2:3] offset0:40 offset1:50
	s_waitcnt vmcnt(17)
	v_cvt_pk_bf16_f32 v0, v24, v25
	v_cvt_pk_bf16_f32 v1, v26, v27
	s_waitcnt vmcnt(16)
	v_cvt_pk_bf16_f32 v2, v28, v29
	v_cvt_pk_bf16_f32 v3, v30, v31
	ds_write2st64_b64 v101, v[0:1], v[2:3] offset0:60 offset1:70
	v_mul_lo_u32 v2, s11, v114
	v_mul_lo_u32 v3, s10, v97
	v_mad_u64_u32 v[0:1], s[10:11], s10, v114, 0
	v_add3_u32 v1, v1, v3, v2
	s_waitcnt lgkmcnt(0)
	s_barrier
	v_lshl_add_u64 v[16:17], v[0:1], 1, s[8:9]
	ds_read_b64_tr_b16 v[0:1], v103
	ds_read_b64_tr_b16 v[2:3], v103 offset:1280
	ds_read_b64_tr_b16 v[4:5], v105
	ds_read_b64_tr_b16 v[6:7], v105 offset:1280
	ds_read_b64_tr_b16 v[8:9], v107
	ds_read_b64_tr_b16 v[10:11], v107 offset:1280
	ds_read_b64_tr_b16 v[12:13], v109
	ds_read_b64_tr_b16 v[14:15], v109 offset:1280
	v_mov_b32_e32 v117, v99
	v_lshl_add_u64 v[16:17], v[16:17], 0, v[116:117]
	s_waitcnt lgkmcnt(6)
	global_store_dwordx4 v[16:17], v[0:3], off
	s_waitcnt lgkmcnt(4)
	global_store_dwordx4 v[16:17], v[4:7], off offset:16
	s_waitcnt lgkmcnt(2)
	global_store_dwordx4 v[16:17], v[8:11], off offset:128
	s_waitcnt lgkmcnt(0)
	global_store_dwordx4 v[16:17], v[12:15], off offset:144
	s_add_i32 s30, s30, 1
	s_cmp_ge_i32 s30, s31
	s_mov_b64 s[10:11], s[18:19]
	s_mov_b64 s[8:9], s[16:17]
	s_barrier
	s_cbranch_scc1 .LBB0_2101

; #define LAS __attribute__((address_space(3)))
; __device__ __forceinline__ unsigned cvt_pk_bf16(float lo, float hi) { const bf16x2_t r = __builtin_convertvector((f32x2_t){lo, hi}, bf16x2_t); return __builtin_bit_cast(unsigned, r); }
; __device__ __forceinline__ void cvt_range(const MkArgs& a, LAS unsigned char* lds, const int tid, const int first, const int step, const int end, const bool deferred) {
;     ...
;         if (tm < end) { cvt_decode(cvt_map(tm, deferred), w_in, w_out, w_eg, w_eu, w_ed, WinT, WoutT, WguT, WdT, srcm, dstm, ldm, Km);
; #pragma unroll
;             for (int i = 0; i < 8; ++i) vm[i] = __builtin_nontemporal_load((const f32x4*)(srcm + (size_t)(kk + 16 * i) * ldm + c4 * 4)); }
; #pragma unroll
;         for (int i = 0; i < 8; ++i) {
;             u32x2 p; p[0] = cvt_pk_bf16(v[i][0], v[i][1]); p[1] = cvt_pk_bf16(v[i][2], v[i][3]);
;             *(LAS u32x2*)(lds + (kk + 16 * i) * RS + c4 * 8) = p;
;         }
;         __syncthreads();
;         {
;             typedef short s16x4_t __attribute__((ext_vector_type(4)));
;             const int ln = tid & 63, wq = tid >> 6, li = ln & 15, gq = li >> 2, gp = li & 3, G4 = ln >> 4;
; #pragma unroll
;             for (int i = 0; i < 4; ++i) {
;                 const int nb = wq, k8 = 2 * (G4 + 4 * (i >> 1)) + (i & 1);
;                 const LAS unsigned char* p0 = lds + (8 * k8 + gq) * RS + (16 * nb + 4 * gp) * 2;
;                 const s16x4_t x0 = __builtin_amdgcn_ds_read_tr16_b64_v4i16((LAS s16x4_t*)p0), x1 = __builtin_amdgcn_ds_read_tr16_b64_v4i16((LAS s16x4_t*)(p0 + 4 * RS));
;                 typedef short s16x8_t __attribute__((ext_vector_type(8)));
;                 const s16x8_t o8 = (s16x8_t){x0[0], x0[1], x0[2], x0[3], x1[0], x1[1], x1[2], x1[3]};
;                 *(u32x4*)(dst + (size_t)(16 * nb + li) * K + k8 * 8) = __builtin_bit_cast(u32x4, o8);
;             }
;         }
;         __syncthreads();
;         t += step; src = srcn; dst = dstn; ld = ldn; K = Kn; srcn = srcm; dstn = dstm; ldn = ldm; Kn = Km;
; #pragma unroll
;         for (int i = 0; i < 8; ++i) { v[i] = vn[i]; vn[i] = vm[i]; }
.Lmy_cv5_1_2122:
	v_lshl_add_u64 v[24:25], s[20:21], 0, v[98:99]
	v_mad_i64_i32 v[0:1], s[20:21], s22, v96, 0
	v_lshl_add_u64 v[8:9], v[0:1], 2, v[24:25]
	v_mad_i64_i32 v[0:1], s[20:21], s22, v100, 0
	v_lshl_add_u64 v[10:11], v[0:1], 2, v[24:25]
	global_load_dwordx4 v[0:3], v[8:9], off nt
	global_load_dwordx4 v[4:7], v[10:11], off nt
	v_mad_i64_i32 v[8:9], s[20:21], s22, v102, 0
	v_mad_i64_i32 v[10:11], s[20:21], s22, v104, 0
	v_mad_i64_i32 v[16:17], s[20:21], s22, v106, 0
	v_mad_i64_i32 v[18:19], s[20:21], s22, v108, 0
	v_mad_i64_i32 v[26:27], s[20:21], s22, v110, 0
	v_mad_i64_i32 v[28:29], s[20:21], s22, v112, 0
	v_lshl_add_u64 v[8:9], v[8:9], 2, v[24:25]
	v_lshl_add_u64 v[12:13], v[10:11], 2, v[24:25]
	v_lshl_add_u64 v[16:17], v[16:17], 2, v[24:25]
	v_lshl_add_u64 v[20:21], v[18:19], 2, v[24:25]
	v_lshl_add_u64 v[26:27], v[26:27], 2, v[24:25]
	v_lshl_add_u64 v[28:29], v[28:29], 2, v[24:25]
	global_load_dwordx4 v[8:11], v[8:9], off nt
	s_nop 0
	global_load_dwordx4 v[12:15], v[12:13], off nt
	s_nop 0
	global_load_dwordx4 v[16:19], v[16:17], off nt
	s_nop 0
	global_load_dwordx4 v[20:23], v[20:21], off nt
	s_nop 0
	global_load_dwordx4 v[24:27], v[26:27], off nt
	s_nop 0
	global_load_dwordx4 v[28:31], v[28:29], off nt
.Lmy_cv5_1_2123:
	s_waitcnt vmcnt(23)
	v_cvt_pk_bf16_f32 v36, v36, v37
	v_cvt_pk_bf16_f32 v37, v38, v39
	s_waitcnt vmcnt(22)
	v_cvt_pk_bf16_f32 v38, v32, v33
	v_cvt_pk_bf16_f32 v39, v34, v35
	ds_write2st64_b64 v101, v[36:37], v[38:39] offset1:10
	s_waitcnt vmcnt(21)
	v_cvt_pk_bf16_f32 v36, v44, v45
	v_cvt_pk_bf16_f32 v37, v46, v47
	s_waitcnt vmcnt(20)
	v_cvt_pk_bf16_f32 v38, v40, v41
	v_cvt_pk_bf16_f32 v39, v42, v43
	ds_write2st64_b64 v101, v[36:37], v[38:39] offset0:20 offset1:30
	s_waitcnt vmcnt(19)
	v_cvt_pk_bf16_f32 v36, v52, v53
	v_cvt_pk_bf16_f32 v37, v54, v55
	s_waitcnt vmcnt(18)
	v_cvt_pk_bf16_f32 v38, v48, v49
	v_cvt_pk_bf16_f32 v39, v50, v51
	ds_write2st64_b64 v101, v[36:37], v[38:39] offset0:40 offset1:50
	s_waitcnt vmcnt(17)
	v_cvt_pk_bf16_f32 v36, v60, v61
	v_cvt_pk_bf16_f32 v37, v62, v63
	s_waitcnt vmcnt(16)
	v_cvt_pk_bf16_f32 v38, v56, v57
	v_cvt_pk_bf16_f32 v39, v58, v59
	ds_write2st64_b64 v101, v[36:37], v[38:39] offset0:60 offset1:70
	v_mul_lo_u32 v38, s11, v114
	v_mul_lo_u32 v39, s10, v97
	v_mad_u64_u32 v[36:37], s[10:11], s10, v114, 0
	v_add3_u32 v37, v37, v39, v38
	s_waitcnt lgkmcnt(0)
	s_barrier
	v_lshl_add_u64 v[52:53], v[36:37], 1, s[8:9]
	ds_read_b64_tr_b16 v[36:37], v103
	ds_read_b64_tr_b16 v[38:39], v103 offset:1280
	ds_read_b64_tr_b16 v[32:33], v105
	ds_read_b64_tr_b16 v[34:35], v105 offset:1280
	ds_read_b64_tr_b16 v[44:45], v107
	ds_read_b64_tr_b16 v[46:47], v107 offset:1280
	ds_read_b64_tr_b16 v[40:41], v109
	ds_read_b64_tr_b16 v[42:43], v109 offset:1280
	v_mov_b32_e32 v117, v99
	v_lshl_add_u64 v[52:53], v[52:53], 0, v[116:117]
	s_waitcnt lgkmcnt(6)
	global_store_dwordx4 v[52:53], v[36:39], off
	s_waitcnt lgkmcnt(4)
	global_store_dwordx4 v[52:53], v[32:35], off offset:16
	s_waitcnt lgkmcnt(2)
	global_store_dwordx4 v[52:53], v[44:47], off offset:128
	s_waitcnt lgkmcnt(0)
	global_store_dwordx4 v[52:53], v[40:43], off offset:144
	s_add_i32 s30, s30, 1
	s_cmp_ge_i32 s30, s31
	s_mov_b64 s[10:11], s[18:19]
	s_mov_b64 s[8:9], s[16:17]
	s_barrier
	s_cbranch_scc1 .LBB0_2101

; #define LAS __attribute__((address_space(3)))
; __device__ __forceinline__ unsigned cvt_pk_bf16(float lo, float hi) { const bf16x2_t r = __builtin_convertvector((f32x2_t){lo, hi}, bf16x2_t); return __builtin_bit_cast(unsigned, r); }
; __device__ __forceinline__ void cvt_range(const MkArgs& a, LAS unsigned char* lds, const int tid, const int first, const int step, const int end, const bool deferred) {
;     ...
;         if (tm < end) { cvt_decode(cvt_map(tm, deferred), w_in, w_out, w_eg, w_eu, w_ed, WinT, WoutT, WguT, WdT, srcm, dstm, ldm, Km);
; #pragma unroll
;             for (int i = 0; i < 8; ++i) vm[i] = __builtin_nontemporal_load((const f32x4*)(srcm + (size_t)(kk + 16 * i) * ldm + c4 * 4)); }
; #pragma unroll
;         for (int i = 0; i < 8; ++i) {
;             u32x2 p; p[0] = cvt_pk_bf16(v[i][0], v[i][1]); p[1] = cvt_pk_bf16(v[i][2], v[i][3]);
;             *(LAS u32x2*)(lds + (kk + 16 * i) * RS + c4 * 8) = p;
;         }
;         __syncthreads();
;         {
;             typedef short s16x4_t __attribute__((ext_vector_type(4)));
;             const int ln = tid & 63, wq = tid >> 6, li = ln & 15, gq = li >> 2, gp = li & 3, G4 = ln >> 4;
; #pragma unroll
;             for (int i = 0; i < 4; ++i) {
;                 const int nb = wq, k8 = 2 * (G4 + 4 * (i >> 1)) + (i & 1);
;                 const LAS unsigned char* p0 = lds + (8 * k8 + gq) * RS + (16 * nb + 4 * gp) * 2;
;                 const s16x4_t x0 = __builtin_amdgcn_ds_read_tr16_b64_v4i16((LAS s16x4_t*)p0), x1 = __builtin_amdgcn_ds_read_tr16_b64_v4i16((LAS s16x4_t*)(p0 + 4 * RS));
;                 typedef short s16x8_t __attribute__((ext_vector_type(8)));
;                 const s16x8_t o8 = (s16x8_t){x0[0], x0[1], x0[2], x0[3], x1[0], x1[1], x1[2], x1[3]};
;                 *(u32x4*)(dst + (size_t)(16 * nb + li) * K + k8 * 8) = __builtin_bit_cast(u32x4, o8);
;             }
;         }
;         __syncthreads();
;         t += step; src = srcn; dst = dstn; ld = ldn; K = Kn; srcn = srcm; dstn = dstm; ldn = ldm; Kn = Km;
; #pragma unroll
;         for (int i = 0; i < 8; ++i) { v[i] = vn[i]; vn[i] = vm[i]; }
.Lmy_cv5_2_2122:
	v_lshl_add_u64 v[60:61], s[20:21], 0, v[98:99]
	v_mad_i64_i32 v[36:37], s[20:21], s22, v96, 0
	v_lshl_add_u64 v[44:45], v[36:37], 2, v[60:61]
	v_mad_i64_i32 v[36:37], s[20:21], s22, v100, 0
	v_lshl_add_u64 v[46:47], v[36:37], 2, v[60:61]
	global_load_dwordx4 v[36:39], v[44:45], off nt
	global_load_dwordx4 v[32:35], v[46:47], off nt
	v_mad_i64_i32 v[44:45], s[20:21], s22, v102, 0
	v_mad_i64_i32 v[46:47], s[20:21], s22, v104, 0
	v_mad_i64_i32 v[52:53], s[20:21], s22, v106, 0
	v_mad_i64_i32 v[54:55], s[20:21], s22, v108, 0
	v_mad_i64_i32 v[62:63], s[20:21], s22, v110, 0
	v_mad_i64_i32 v[56:57], s[20:21], s22, v112, 0
	v_lshl_add_u64 v[44:45], v[44:45], 2, v[60:61]
	v_lshl_add_u64 v[40:41], v[46:47], 2, v[60:61]
	v_lshl_add_u64 v[52:53], v[52:53], 2, v[60:61]
	v_lshl_add_u64 v[48:49], v[54:55], 2, v[60:61]
	v_lshl_add_u64 v[62:63], v[62:63], 2, v[60:61]
	v_lshl_add_u64 v[56:57], v[56:57], 2, v[60:61]
	global_load_dwordx4 v[44:47], v[44:45], off nt
	s_nop 0
	global_load_dwordx4 v[40:43], v[40:41], off nt
	s_nop 0
	global_load_dwordx4 v[52:55], v[52:53], off nt
	s_nop 0
	global_load_dwordx4 v[48:51], v[48:49], off nt
	s_nop 0
	global_load_dwordx4 v[60:63], v[62:63], off nt
	s_nop 0
	global_load_dwordx4 v[56:59], v[56:57], off nt
.Lmy_cv5_2_2123:
	s_waitcnt vmcnt(23)
	v_cvt_pk_bf16_f32 v64, v64, v65
	v_cvt_pk_bf16_f32 v65, v66, v67
	s_waitcnt vmcnt(22)
	v_cvt_pk_bf16_f32 v66, v68, v69
	v_cvt_pk_bf16_f32 v67, v70, v71
	ds_write2st64_b64 v101, v[64:65], v[66:67] offset1:10
	s_waitcnt vmcnt(21)
	v_cvt_pk_bf16_f32 v64, v72, v73
	v_cvt_pk_bf16_f32 v65, v74, v75
	s_waitcnt vmcnt(20)
	v_cvt_pk_bf16_f32 v66, v76, v77
	v_cvt_pk_bf16_f32 v67, v78, v79
	ds_write2st64_b64 v101, v[64:65], v[66:67] offset0:20 offset1:30
	s_waitcnt vmcnt(19)
	v_cvt_pk_bf16_f32 v64, v80, v81
	v_cvt_pk_bf16_f32 v65, v82, v83
	s_waitcnt vmcnt(18)
	v_cvt_pk_bf16_f32 v66, v84, v85
	v_cvt_pk_bf16_f32 v67, v86, v87
	ds_write2st64_b64 v101, v[64:65], v[66:67] offset0:40 offset1:50
	s_waitcnt vmcnt(17)
	v_cvt_pk_bf16_f32 v64, v88, v89
	v_cvt_pk_bf16_f32 v65, v90, v91
	s_waitcnt vmcnt(16)
	v_cvt_pk_bf16_f32 v66, v92, v93
	v_cvt_pk_bf16_f32 v67, v94, v95
	ds_write2st64_b64 v101, v[64:65], v[66:67] offset0:60 offset1:70
	v_mul_lo_u32 v66, s11, v114
	v_mul_lo_u32 v67, s10, v97
	v_mad_u64_u32 v[64:65], s[10:11], s10, v114, 0
	v_add3_u32 v65, v65, v67, v66
	s_waitcnt lgkmcnt(0)
	s_barrier
	v_lshl_add_u64 v[80:81], v[64:65], 1, s[8:9]
	ds_read_b64_tr_b16 v[64:65], v103
	ds_read_b64_tr_b16 v[66:67], v103 offset:1280
	ds_read_b64_tr_b16 v[68:69], v105
	ds_read_b64_tr_b16 v[70:71], v105 offset:1280
	ds_read_b64_tr_b16 v[72:73], v107
	ds_read_b64_tr_b16 v[74:75], v107 offset:1280
	ds_read_b64_tr_b16 v[76:77], v109
	ds_read_b64_tr_b16 v[78:79], v109 offset:1280
	v_mov_b32_e32 v117, v99
	v_lshl_add_u64 v[80:81], v[80:81], 0, v[116:117]
	s_waitcnt lgkmcnt(6)
	global_store_dwordx4 v[80:81], v[64:67], off
	s_waitcnt lgkmcnt(4)
	global_store_dwordx4 v[80:81], v[68:71], off offset:16
	s_waitcnt lgkmcnt(2)
	global_store_dwordx4 v[80:81], v[72:75], off offset:128
	s_waitcnt lgkmcnt(0)
	global_store_dwordx4 v[80:81], v[76:79], off offset:144
	s_add_i32 s30, s30, 1
	s_cmp_ge_i32 s30, s31
	s_mov_b64 s[10:11], s[18:19]
	s_mov_b64 s[8:9], s[16:17]
	s_barrier
	s_cbranch_scc1 .LBB0_2101
